# baseline (speedup 1.0000x reference)
_Z8attn_fwdPKfPKiPf:
	s_load_dwordx4 s[4:7], s[0:1], 0x0
	s_load_dwordx2 s[12:13], s[0:1], 0x10
	v_and_b32_e32 v235, 63, v0
	v_lshrrev_b32_e32 v236, 4, v0
	v_and_b32_e32 v237, 15, v0
	v_readfirstlane_b32 s17, v0
	s_nop 3
	s_lshr_b32 s17, s17, 6
	v_mul_u32_u24_e32 v229, 0x3000, v236
	v_lshl_add_u32 v229, v237, 4, v229
	v_lshlrev_b32_e32 v230, 2, v235
	v_add_u32_e32 v245, 0x3000, v230
	v_add_u32_e32 v246, 0x6000, v230
	v_add_u32_e32 v247, 0x9000, v230
	v_add_u32_e32 v248, 0x18000, v230
	v_add_u32_e32 v249, 0x1b000, v230
	v_add_u32_e32 v250, 0x1e000, v230
	v_add_u32_e32 v251, 0x21000, v230
	v_add_u32_e32 v252, 0x60000, v229
	v_and_b32_e32 v238, 31, v0
	v_bfe_u32 v234, v0, 5, 1
	v_lshrrev_b32_e32 v231, 4, v235
	v_mul_u32_u24_e32 v243, 0x3000, v231
	v_lshl_add_u32 v243, v237, 4, v243
	s_and_b32 s33, s2, 7
	s_lshr_b32 s31, s2, 3
	s_and_b32 s39, s31, 3
	s_lshr_b32 s40, s31, 3
	s_lshr_b32 s41, s31, 2
	s_and_b32 s41, s41, 1
	s_lshl_b32 s33, s33, 1
	s_add_u32 s41, s41, s33
	s_mul_i32 s16, s40, 0x1800000
	s_lshl_b32 s31, s41, 8
	s_add_u32 s16, s16, s31
	s_add_u32 s18, s16, 4096
	s_lshr_b32 s31, s17, 1
	s_lshl_b32 s31, s31, 4
	s_and_b32 s33, s17, 1
	s_lshl_b32 s33, s33, 2
	s_add_u32 s31, s31, s33
	s_mul_i32 s31, s31, 0x3000
	s_add_u32 s19, s16, 8192
	s_add_u32 s19, s19, s31
	s_lshl_b32 s22, s40, 13
	s_lshl_b32 s31, s39, 8
	s_lshl_b32 s33, s17, 5
	s_add_u32 s31, s31, s33
	s_mul_i32 s29, s31, 0x3000
	s_add_u32 s29, s29, s16
	s_lshl_b32 s33, s40, 11
	s_add_u32 s31, s31, s33
	s_lshl_b32 s30, s31, 12
	s_lshl_b32 s31, s41, 8
	s_add_u32 s30, s30, s31
	s_mov_b32 s37, 0x46800000
	s_mov_b32 s38, 0xbf800000
	s_mov_b32 s34, 0x46800000
	s_mov_b32 s35, 0xc6616bcd
	s_mov_b32 s36, 0x3e38aa3b
	s_mov_b32 s23, 0
	s_mov_b32 s27, 0
	s_mov_b32 s42, 0
	s_waitcnt lgkmcnt(0)
	s_mov_b32 s8, s6
	s_and_b32 s9, s7, 0xffff
	s_mov_b32 s10, 0x7fffffff
	s_mov_b32 s11, 0x20000
	s_and_b32 s5, s5, 0xffff
	s_mov_b32 s6, 0x7fffffff
	s_mov_b32 s7, 0x20000
	s_and_b32 s13, s13, 0xffff
	s_mov_b32 s14, 0x7fffffff
	s_mov_b32 s15, 0x20000
	s_add_u32 s31, s18, 0x0
	buffer_load_dwordx4 v[64:67], v229, s[4:7], s31 offen
	s_add_u32 s31, s18, 0x60000
	buffer_load_dwordx4 v[68:71], v229, s[4:7], s31 offen
	buffer_load_dword v224, v230, s[8:11], s22 offen
	s_add_u32 s31, s18, 0xc0000
	buffer_load_dwordx4 v[72:75], v229, s[4:7], s31 offen
	s_add_u32 s31, s18, 0x120000
	buffer_load_dwordx4 v[76:79], v229, s[4:7], s31 offen
	s_add_u32 s31, s19, 0x0
	buffer_load_dword v80, v230, s[4:7], s31 offen
	s_add_u32 s31, s19, 0x3000
	buffer_load_dword v81, v230, s[4:7], s31 offen
	s_add_u32 s31, s19, 0x6000
	buffer_load_dword v82, v230, s[4:7], s31 offen
	s_add_u32 s31, s19, 0x9000
	buffer_load_dword v83, v230, s[4:7], s31 offen
	s_add_u32 s31, s19, 0x18000
	buffer_load_dword v84, v230, s[4:7], s31 offen
	s_add_u32 s31, s19, 0x1b000
	buffer_load_dword v85, v230, s[4:7], s31 offen
	s_add_u32 s31, s19, 0x1e000
	buffer_load_dword v86, v230, s[4:7], s31 offen
	s_add_u32 s31, s19, 0x21000
	buffer_load_dword v87, v230, s[4:7], s31 offen
	s_add_u32 s31, s29, 0x0
	buffer_load_dwordx4 v[0:3], v243, s[4:7], s31 offen nt
	s_add_u32 s31, s29, 0xc000
	buffer_load_dwordx4 v[4:7], v243, s[4:7], s31 offen nt
	s_add_u32 s31, s29, 0x18000
	buffer_load_dwordx4 v[8:11], v243, s[4:7], s31 offen nt
	s_add_u32 s31, s29, 0x24000
	buffer_load_dwordx4 v[12:15], v243, s[4:7], s31 offen nt
	s_add_u32 s31, s29, 0x30000
	buffer_load_dwordx4 v[16:19], v243, s[4:7], s31 offen nt
	s_add_u32 s31, s29, 0x3c000
	buffer_load_dwordx4 v[20:23], v243, s[4:7], s31 offen nt
	s_add_u32 s31, s29, 0x48000
	buffer_load_dwordx4 v[24:27], v243, s[4:7], s31 offen nt
	s_add_u32 s31, s29, 0x54000
	buffer_load_dwordx4 v[28:31], v243, s[4:7], s31 offen nt
	v_mul_u32_u24_e32 v227, 144, v236
	v_lshl_add_u32 v227, v237, 3, v227
	v_mov_b32_e32 v236, v234
	v_mul_u32_u24_e32 v225, 144, v238
	v_lshl_add_u32 v225, v236, 4, v225
	v_add_u32_e32 v226, 36864, v225
	v_lshlrev_b32_e32 v234, 2, v236
	v_mul_u32_u24_e32 v228, 144, v235
	s_lshl_b32 s31, s17, 4
	s_add_u32 s31, s31, 36864
	v_add_u32_e32 v228, s31, v228
	s_mul_i32 s32, s17, 8704
	s_add_u32 s32, s32, 73728
	v_mul_u32_u24_e32 v239, 144, v231
	v_lshl_add_u32 v239, v237, 3, v239
	v_add_u32_e32 v239, s32, v239
	v_add_u32_e32 v240, s32, v225
	v_mul_u32_u24_e32 v241, 272, v238
	v_lshl_add_u32 v241, v236, 4, v241
	v_add_u32_e32 v241, s32, v241
	v_mul_u32_u24_e32 v242, 272, v231
	v_lshl_add_u32 v242, v237, 4, v242
	v_add_u32_e32 v242, s32, v242
	v_lshlrev_b32_e32 v244, 12, v231
	v_lshl_add_u32 v244, v237, 4, v244
	s_waitcnt vmcnt(8)
	v_cvt_pk_f16_f32 v64, v64, v65
	v_cvt_pk_f16_f32 v65, v66, v67
	ds_write_b64 v227, v[64:65] offset:0
	v_cvt_pk_f16_f32 v68, v68, v69
	v_cvt_pk_f16_f32 v69, v70, v71
	ds_write_b64 v227, v[68:69] offset:4608
	v_cvt_pk_f16_f32 v72, v72, v73
	v_cvt_pk_f16_f32 v73, v74, v75
	ds_write_b64 v227, v[72:73] offset:9216
	v_cvt_pk_f16_f32 v76, v76, v77
	v_cvt_pk_f16_f32 v77, v78, v79
	ds_write_b64 v227, v[76:77] offset:13824
	v_cvt_pk_f16_f32 v80, v80, v81
	v_cvt_pk_f16_f32 v81, v82, v83
	v_cvt_pk_f16_f32 v82, v84, v85
	v_cvt_pk_f16_f32 v83, v86, v87
	ds_write_b128 v228, v[80:83] offset:0
	s_add_u32 s31, s18, 0x180000
	buffer_load_dwordx4 v[208:211], v229, s[4:7], s31 offen
	s_add_u32 s31, s18, 0x1e0000
	buffer_load_dwordx4 v[212:215], v229, s[4:7], s31 offen
	s_add_u32 s31, s19, 0xc0000
	buffer_load_dword v216, v230, s[4:7], s31 offen
	s_add_u32 s31, s19, 0xc3000
	buffer_load_dword v217, v230, s[4:7], s31 offen
	s_add_u32 s31, s19, 0xc6000
	buffer_load_dword v218, v230, s[4:7], s31 offen
	s_add_u32 s31, s19, 0xc9000
	buffer_load_dword v219, v230, s[4:7], s31 offen
	s_add_u32 s31, s19, 0xd8000
	buffer_load_dword v220, v230, s[4:7], s31 offen
	s_add_u32 s31, s19, 0xdb000
	buffer_load_dword v221, v230, s[4:7], s31 offen
	s_add_u32 s31, s19, 0xde000
	buffer_load_dword v222, v230, s[4:7], s31 offen
	s_add_u32 s31, s19, 0xe1000
	buffer_load_dword v223, v230, s[4:7], s31 offen
	s_waitcnt vmcnt(10)
	v_mul_f32_e32 v0, s36, v0
	v_mul_f32_e32 v1, s36, v1
	v_mul_f32_e32 v2, s36, v2
	v_mul_f32_e32 v3, s36, v3
	v_cvt_pk_f16_f32 v0, v0, v1
	v_cvt_pk_f16_f32 v1, v2, v3
	ds_write_b64 v239, v[0:1] offset:0
	v_mul_f32_e32 v4, s36, v4
	v_mul_f32_e32 v5, s36, v5
	v_mul_f32_e32 v6, s36, v6
	v_mul_f32_e32 v7, s36, v7
	v_cvt_pk_f16_f32 v4, v4, v5
	v_cvt_pk_f16_f32 v5, v6, v7
	ds_write_b64 v239, v[4:5] offset:576
	v_mul_f32_e32 v8, s36, v8
	v_mul_f32_e32 v9, s36, v9
	v_mul_f32_e32 v10, s36, v10
	v_mul_f32_e32 v11, s36, v11
	v_cvt_pk_f16_f32 v8, v8, v9
	v_cvt_pk_f16_f32 v9, v10, v11
	ds_write_b64 v239, v[8:9] offset:1152
	v_mul_f32_e32 v12, s36, v12
	v_mul_f32_e32 v13, s36, v13
	v_mul_f32_e32 v14, s36, v14
	v_mul_f32_e32 v15, s36, v15
	v_cvt_pk_f16_f32 v12, v12, v13
	v_cvt_pk_f16_f32 v13, v14, v15
	ds_write_b64 v239, v[12:13] offset:1728
	v_mul_f32_e32 v16, s36, v16
	v_mul_f32_e32 v17, s36, v17
	v_mul_f32_e32 v18, s36, v18
	v_mul_f32_e32 v19, s36, v19
	v_cvt_pk_f16_f32 v16, v16, v17
	v_cvt_pk_f16_f32 v17, v18, v19
	ds_write_b64 v239, v[16:17] offset:2304
	v_mul_f32_e32 v20, s36, v20
	v_mul_f32_e32 v21, s36, v21
	v_mul_f32_e32 v22, s36, v22
	v_mul_f32_e32 v23, s36, v23
	v_cvt_pk_f16_f32 v20, v20, v21
	v_cvt_pk_f16_f32 v21, v22, v23
	ds_write_b64 v239, v[20:21] offset:2880
	v_mul_f32_e32 v24, s36, v24
	v_mul_f32_e32 v25, s36, v25
	v_mul_f32_e32 v26, s36, v26
	v_mul_f32_e32 v27, s36, v27
	v_cvt_pk_f16_f32 v24, v24, v25
	v_cvt_pk_f16_f32 v25, v26, v27
	ds_write_b64 v239, v[24:25] offset:3456
	v_mul_f32_e32 v28, s36, v28
	v_mul_f32_e32 v29, s36, v29
	v_mul_f32_e32 v30, s36, v30
	v_mul_f32_e32 v31, s36, v31
	v_cvt_pk_f16_f32 v28, v28, v29
	v_cvt_pk_f16_f32 v29, v30, v31
	ds_write_b64 v239, v[28:29] offset:4032
	s_waitcnt lgkmcnt(0)
	ds_read_b128 v[128:131], v240 offset:0
	ds_read_b128 v[132:135], v240 offset:32
	ds_read_b128 v[136:139], v240 offset:64
	ds_read_b128 v[140:143], v240 offset:96
	s_waitcnt lgkmcnt(0)
	s_barrier
	ds_read_b128 v[176:179], v225 offset:0
	ds_read_b128 v[180:183], v225 offset:32
	ds_read_b128 v[184:187], v225 offset:64
	ds_read_b128 v[188:191], v225 offset:96
	ds_read_b128 v[192:195], v225 offset:4608
	ds_read_b128 v[196:199], v225 offset:4640
	ds_read_b128 v[200:203], v225 offset:4672
	ds_read_b128 v[204:207], v225 offset:4704
	s_waitcnt lgkmcnt(0)
	v_cmp_ne_u32_e64 s[20:21], 0, v224
	v_mfma_f32_32x32x16_f16 v[64:79], v[176:179], v[128:131], 0
	v_mfma_f32_32x32x16_f16 v[64:79], v[180:183], v[132:135], v[64:79]
	v_mfma_f32_32x32x16_f16 v[64:79], v[184:187], v[136:139], v[64:79]
	v_mfma_f32_32x32x16_f16 v[64:79], v[188:191], v[140:143], v[64:79]
	v_mfma_f32_32x32x16_f16 v[80:95], v[192:195], v[128:131], 0
	v_mfma_f32_32x32x16_f16 v[80:95], v[196:199], v[132:135], v[80:95]
	v_mfma_f32_32x32x16_f16 v[80:95], v[200:203], v[136:139], v[80:95]
	v_mfma_f32_32x32x16_f16 v[80:95], v[204:207], v[140:143], v[80:95]
	s_nop 15
	s_nop 3
	s_cmp_eq_u64 s[20:21], -1
	s_cbranch_scc1 .Lpro_nomask_A
	v_lshrrev_b32_e64 v235, v234, s20
	v_bfe_u32 v236, v235, 0, 1
	v_cvt_f32_u32_e32 v236, v236
	v_sub_f32_e32 v236, 1.0, v236
	v_fmac_f32_e32 v64, s35, v236
	v_bfe_u32 v236, v235, 1, 1
	v_cvt_f32_u32_e32 v236, v236
	v_sub_f32_e32 v236, 1.0, v236
	v_fmac_f32_e32 v65, s35, v236
	v_bfe_u32 v236, v235, 2, 1
	v_cvt_f32_u32_e32 v236, v236
	v_sub_f32_e32 v236, 1.0, v236
	v_fmac_f32_e32 v66, s35, v236
	v_bfe_u32 v236, v235, 3, 1
	v_cvt_f32_u32_e32 v236, v236
	v_sub_f32_e32 v236, 1.0, v236
	v_fmac_f32_e32 v67, s35, v236
	v_bfe_u32 v236, v235, 8, 1
	v_cvt_f32_u32_e32 v236, v236
	v_sub_f32_e32 v236, 1.0, v236
	v_fmac_f32_e32 v68, s35, v236
	v_bfe_u32 v236, v235, 9, 1
	v_cvt_f32_u32_e32 v236, v236
	v_sub_f32_e32 v236, 1.0, v236
	v_fmac_f32_e32 v69, s35, v236
	v_bfe_u32 v236, v235, 10, 1
	v_cvt_f32_u32_e32 v236, v236
	v_sub_f32_e32 v236, 1.0, v236
	v_fmac_f32_e32 v70, s35, v236
	v_bfe_u32 v236, v235, 11, 1
	v_cvt_f32_u32_e32 v236, v236
	v_sub_f32_e32 v236, 1.0, v236
	v_fmac_f32_e32 v71, s35, v236
	v_bfe_u32 v236, v235, 16, 1
	v_cvt_f32_u32_e32 v236, v236
	v_sub_f32_e32 v236, 1.0, v236
	v_fmac_f32_e32 v72, s35, v236
	v_bfe_u32 v236, v235, 17, 1
	v_cvt_f32_u32_e32 v236, v236
	v_sub_f32_e32 v236, 1.0, v236
	v_fmac_f32_e32 v73, s35, v236
	v_bfe_u32 v236, v235, 18, 1
	v_cvt_f32_u32_e32 v236, v236
	v_sub_f32_e32 v236, 1.0, v236
	v_fmac_f32_e32 v74, s35, v236
	v_bfe_u32 v236, v235, 19, 1
	v_cvt_f32_u32_e32 v236, v236
	v_sub_f32_e32 v236, 1.0, v236
	v_fmac_f32_e32 v75, s35, v236
	v_bfe_u32 v236, v235, 24, 1
	v_cvt_f32_u32_e32 v236, v236
	v_sub_f32_e32 v236, 1.0, v236
	v_fmac_f32_e32 v76, s35, v236
	v_bfe_u32 v236, v235, 25, 1
	v_cvt_f32_u32_e32 v236, v236
	v_sub_f32_e32 v236, 1.0, v236
	v_fmac_f32_e32 v77, s35, v236
	v_bfe_u32 v236, v235, 26, 1
	v_cvt_f32_u32_e32 v236, v236
	v_sub_f32_e32 v236, 1.0, v236
	v_fmac_f32_e32 v78, s35, v236
	v_bfe_u32 v236, v235, 27, 1
	v_cvt_f32_u32_e32 v236, v236
	v_sub_f32_e32 v236, 1.0, v236
	v_fmac_f32_e32 v79, s35, v236
	v_lshrrev_b32_e64 v235, v234, s21
	v_bfe_u32 v236, v235, 0, 1
	v_cvt_f32_u32_e32 v236, v236
	v_sub_f32_e32 v236, 1.0, v236
	v_fmac_f32_e32 v80, s35, v236
	v_bfe_u32 v236, v235, 1, 1
	v_cvt_f32_u32_e32 v236, v236
	v_sub_f32_e32 v236, 1.0, v236
	v_fmac_f32_e32 v81, s35, v236
	v_bfe_u32 v236, v235, 2, 1
	v_cvt_f32_u32_e32 v236, v236
	v_sub_f32_e32 v236, 1.0, v236
	v_fmac_f32_e32 v82, s35, v236
	v_bfe_u32 v236, v235, 3, 1
	v_cvt_f32_u32_e32 v236, v236
	v_sub_f32_e32 v236, 1.0, v236
	v_fmac_f32_e32 v83, s35, v236
	v_bfe_u32 v236, v235, 8, 1
	v_cvt_f32_u32_e32 v236, v236
	v_sub_f32_e32 v236, 1.0, v236
	v_fmac_f32_e32 v84, s35, v236
	v_bfe_u32 v236, v235, 9, 1
	v_cvt_f32_u32_e32 v236, v236
	v_sub_f32_e32 v236, 1.0, v236
	v_fmac_f32_e32 v85, s35, v236
	v_bfe_u32 v236, v235, 10, 1
	v_cvt_f32_u32_e32 v236, v236
	v_sub_f32_e32 v236, 1.0, v236
	v_fmac_f32_e32 v86, s35, v236
	v_bfe_u32 v236, v235, 11, 1
	v_cvt_f32_u32_e32 v236, v236
	v_sub_f32_e32 v236, 1.0, v236
	v_fmac_f32_e32 v87, s35, v236
	v_bfe_u32 v236, v235, 16, 1
	v_cvt_f32_u32_e32 v236, v236
	v_sub_f32_e32 v236, 1.0, v236
	v_fmac_f32_e32 v88, s35, v236
	v_bfe_u32 v236, v235, 17, 1
	v_cvt_f32_u32_e32 v236, v236
	v_sub_f32_e32 v236, 1.0, v236
	v_fmac_f32_e32 v89, s35, v236
	v_bfe_u32 v236, v235, 18, 1
	v_cvt_f32_u32_e32 v236, v236
	v_sub_f32_e32 v236, 1.0, v236
	v_fmac_f32_e32 v90, s35, v236
	v_bfe_u32 v236, v235, 19, 1
	v_cvt_f32_u32_e32 v236, v236
	v_sub_f32_e32 v236, 1.0, v236
	v_fmac_f32_e32 v91, s35, v236
	v_bfe_u32 v236, v235, 24, 1
	v_cvt_f32_u32_e32 v236, v236
	v_sub_f32_e32 v236, 1.0, v236
	v_fmac_f32_e32 v92, s35, v236
	v_bfe_u32 v236, v235, 25, 1
	v_cvt_f32_u32_e32 v236, v236
	v_sub_f32_e32 v236, 1.0, v236
	v_fmac_f32_e32 v93, s35, v236
	v_bfe_u32 v236, v235, 26, 1
	v_cvt_f32_u32_e32 v236, v236
	v_sub_f32_e32 v236, 1.0, v236
	v_fmac_f32_e32 v94, s35, v236
	v_bfe_u32 v236, v235, 27, 1
	v_cvt_f32_u32_e32 v236, v236
	v_sub_f32_e32 v236, 1.0, v236
	v_fmac_f32_e32 v95, s35, v236

.Lnoprio:
	s_waitcnt vmcnt(8)
	v_cmp_ne_u32_e64 s[20:21], 0, v224
	s_add_u32 s31, s23, 1
	s_and_b32 s31, s31, 31
	s_lshl_b32 s31, s31, 8
	s_add_u32 s26, s31, s22
	s_add_u32 s31, s23, 3
	s_and_b32 s31, s31, 31
	s_mul_i32 s31, s31, 0xc0000
	s_add_u32 s24, s31, s18
	s_add_u32 s31, s23, 2
	s_and_b32 s31, s31, 31
	s_mul_i32 s31, s31, 0xc0000
	s_add_u32 s25, s31, s19
	s_cmp_eq_u64 s[20:21], -1
	s_cselect_b32 s34, s37, s38
	ds_read_b128 v[176:179], v225 offset:9216
	s_add_u32 s31, s29, 0xc00000
	buffer_load_dwordx4 v[32:35], v243, s[4:7], s31 offen nt
	s_add_u32 s31, s29, 0xc0c000
	buffer_load_dwordx4 v[36:39], v243, s[4:7], s31 offen nt
	buffer_load_dword v224, v230, s[8:11], s26 offen
	v_exp_f32_e32 v64, v64
	v_exp_f32_e32 v65, v65
	v_cvt_pk_f16_f32 v208, v208, v209
	v_cvt_pk_f16_f32 v209, v210, v211
	ds_read_b128 v[180:183], v225 offset:9248
	v_exp_f32_e32 v66, v66
	v_exp_f32_e32 v67, v67
	v_cvt_pk_f16_f32 v212, v212, v213
	v_cvt_pk_f16_f32 v160, v64, v65
	v_add_f32_e32 v64, v64, v65
	v_cvt_pk_f16_f32 v213, v214, v215
	ds_write_b64 v227, v[208:209] offset:18432
	ds_write_b64 v227, v[212:213] offset:23040
	ds_read_b128 v[184:187], v225 offset:9280
	v_exp_f32_e32 v68, v68
	v_exp_f32_e32 v69, v69
	v_cvt_pk_f16_f32 v161, v66, v67
	v_add_f32_e32 v66, v66, v67
	ds_read_b128 v[188:191], v225 offset:9312
	buffer_load_dwordx4 v[208:211], v229, s[4:7], s24 offen
	v_exp_f32_e32 v70, v70
	v_exp_f32_e32 v71, v71
	v_cvt_pk_f16_f32 v162, v68, v69
	v_add_f32_e32 v68, v68, v69
	v_add_f32_e32 v231, v64, v66
	ds_read_b128 v[192:195], v226 offset:0
	buffer_load_dwordx4 v[212:215], v252, s[4:7], s24 offen
	v_exp_f32_e32 v72, v72
	v_exp_f32_e32 v73, v73
	v_cvt_pk_f16_f32 v163, v70, v71
	v_add_f32_e32 v70, v70, v71
	v_add_f32_e32 v231, v231, v68
	ds_read_b128 v[196:199], v226 offset:4608
	v_exp_f32_e32 v74, v74
	v_exp_f32_e32 v75, v75
	v_cvt_pk_f16_f32 v164, v72, v73
	v_add_f32_e32 v72, v72, v73
	v_add_f32_e32 v231, v231, v70
	ds_read_b128 v[200:203], v226 offset:32
	v_exp_f32_e32 v76, v76
	v_exp_f32_e32 v77, v77
	v_cvt_pk_f16_f32 v165, v74, v75
	v_add_f32_e32 v74, v74, v75
	v_add_f32_e32 v231, v231, v72
	ds_read_b128 v[204:207], v226 offset:4640
	v_exp_f32_e32 v78, v78
	v_exp_f32_e32 v79, v79
	v_cvt_pk_f16_f32 v166, v76, v77
	v_add_f32_e32 v76, v76, v77
	v_add_f32_e32 v231, v231, v74
	v_cvt_pk_f16_f32 v167, v78, v79
	v_add_f32_e32 v78, v78, v79
	v_add_f32_e32 v231, v231, v76
	v_add_f32_e32 v231, v231, v78
	v_cmp_nge_f32_e32 vcc, s34, v231
	s_cbranch_vccnz .Lovf_a1_00
.Lovfret_a1_00:
	v_add_f32_e32 v232, v232, v231
	s_waitcnt lgkmcnt(4)
	v_mfma_f32_32x32x16_f16 v[64:79], v[176:179], v[128:131], v[96:111]
	ds_read_b128 v[176:179], v225 offset:13824
	s_waitcnt vmcnt(5)
	v_exp_f32_e32 v80, v80
	v_exp_f32_e32 v81, v81
	v_cvt_pk_f16_f32 v216, v216, v217
	v_cvt_pk_f16_f32 v217, v218, v219
	v_mfma_f32_32x32x16_f16 v[64:79], v[180:183], v[132:135], v[64:79]
	ds_read_b128 v[180:183], v225 offset:13856
	v_exp_f32_e32 v82, v82
	v_exp_f32_e32 v83, v83
	v_cvt_pk_f16_f32 v218, v220, v221
	v_cvt_pk_f16_f32 v168, v80, v81
	v_add_f32_e32 v80, v80, v81
	v_cvt_pk_f16_f32 v219, v222, v223
	v_mfma_f32_32x32x16_f16 v[64:79], v[184:187], v[136:139], v[64:79]
	ds_write_b128 v228, v[216:219] offset:9216
	ds_read_b128 v[184:187], v225 offset:13888
	v_exp_f32_e32 v84, v84
	v_exp_f32_e32 v85, v85
	v_cvt_pk_f16_f32 v169, v82, v83
	v_add_f32_e32 v82, v82, v83
	v_mfma_f32_32x32x16_f16 v[64:79], v[188:191], v[140:143], v[64:79]
	ds_read_b128 v[188:191], v225 offset:13920
	buffer_load_dword v216, v230, s[4:7], s25 offen
	buffer_load_dword v217, v245, s[4:7], s25 offen
	v_exp_f32_e32 v86, v86
	v_exp_f32_e32 v87, v87
	v_cvt_pk_f16_f32 v170, v84, v85
	v_add_f32_e32 v84, v84, v85
	v_add_f32_e32 v231, v80, v82
	s_waitcnt lgkmcnt(5)
	v_mfma_f32_32x32x16_f16 v[0:15], v[192:195], v[160:163], v[0:15]
	ds_read_b128 v[192:195], v226 offset:64
	buffer_load_dword v218, v246, s[4:7], s25 offen
	buffer_load_dword v219, v247, s[4:7], s25 offen
	v_exp_f32_e32 v88, v88
	v_exp_f32_e32 v89, v89
	v_cvt_pk_f16_f32 v171, v86, v87
	v_add_f32_e32 v86, v86, v87
	v_add_f32_e32 v231, v231, v84
	v_mfma_f32_32x32x16_f16 v[16:31], v[196:199], v[160:163], v[16:31]
	ds_read_b128 v[196:199], v226 offset:4672
	buffer_load_dword v220, v248, s[4:7], s25 offen
	buffer_load_dword v221, v249, s[4:7], s25 offen
	v_exp_f32_e32 v90, v90
	v_exp_f32_e32 v91, v91
	v_cvt_pk_f16_f32 v172, v88, v89
	v_add_f32_e32 v88, v88, v89
	v_add_f32_e32 v231, v231, v86
	v_mfma_f32_32x32x16_f16 v[0:15], v[200:203], v[164:167], v[0:15]
	ds_read_b128 v[200:203], v226 offset:96
	buffer_load_dword v222, v250, s[4:7], s25 offen
	v_exp_f32_e32 v92, v92
	v_exp_f32_e32 v93, v93
	v_cvt_pk_f16_f32 v173, v90, v91
	v_add_f32_e32 v90, v90, v91
	v_add_f32_e32 v231, v231, v88
	v_mfma_f32_32x32x16_f16 v[16:31], v[204:207], v[164:167], v[16:31]
	ds_read_b128 v[204:207], v226 offset:4704
	buffer_load_dword v223, v251, s[4:7], s25 offen
	v_exp_f32_e32 v94, v94
	v_exp_f32_e32 v95, v95
	v_cvt_pk_f16_f32 v174, v92, v93
	v_add_f32_e32 v92, v92, v93
	v_add_f32_e32 v231, v231, v90
	v_cvt_pk_f16_f32 v175, v94, v95
	v_add_f32_e32 v94, v94, v95
	v_add_f32_e32 v231, v231, v92
	v_add_f32_e32 v231, v231, v94
	v_cmp_nge_f32_e32 vcc, s34, v231
	s_cbranch_vccnz .Lovf_a1_01
.Lovfret_a1_01:
	v_add_f32_e32 v232, v232, v231
	s_waitcnt lgkmcnt(6)
	s_barrier
	s_add_u32 s23, s23, 1
	s_waitcnt vmcnt(8)
	v_cmp_ne_u32_e64 s[20:21], 0, v224
	s_add_u32 s31, s23, 1
	s_and_b32 s31, s31, 31
	s_lshl_b32 s31, s31, 8
	s_add_u32 s26, s31, s22
	s_add_u32 s31, s23, 3
	s_and_b32 s31, s31, 31
	s_mul_i32 s31, s31, 0xc0000
	s_add_u32 s24, s31, s18
	s_add_u32 s31, s23, 2
	s_and_b32 s31, s31, 31
	s_mul_i32 s31, s31, 0xc0000
	s_add_u32 s25, s31, s19
	s_cmp_eq_u64 s[20:21], -1
	s_cselect_b32 s34, s37, s38
	s_waitcnt lgkmcnt(4)
	v_mfma_f32_32x32x16_f16 v[80:95], v[176:179], v[128:131], v[96:111]
	ds_read_b128 v[176:179], v225 offset:18432
	s_add_u32 s31, s29, 0xc18000
	buffer_load_dwordx4 v[40:43], v243, s[4:7], s31 offen nt
	s_add_u32 s31, s29, 0xc24000
	buffer_load_dwordx4 v[44:47], v243, s[4:7], s31 offen nt
	buffer_load_dword v224, v230, s[8:11], s26 offen
	v_exp_f32_e32 v64, v64
	v_exp_f32_e32 v65, v65
	v_cvt_pk_f16_f32 v208, v208, v209
	v_cvt_pk_f16_f32 v209, v210, v211
	v_mfma_f32_32x32x16_f16 v[80:95], v[180:183], v[132:135], v[80:95]
	ds_read_b128 v[180:183], v225 offset:18464
	v_exp_f32_e32 v66, v66
	v_exp_f32_e32 v67, v67
	v_cvt_pk_f16_f32 v212, v212, v213
	v_cvt_pk_f16_f32 v160, v64, v65
	v_add_f32_e32 v64, v64, v65
	v_cvt_pk_f16_f32 v213, v214, v215
	v_mfma_f32_32x32x16_f16 v[80:95], v[184:187], v[136:139], v[80:95]
	ds_write_b64 v227, v[208:209] offset:27648
	ds_write_b64 v227, v[212:213] offset:32256
	ds_read_b128 v[184:187], v225 offset:18496
	v_exp_f32_e32 v68, v68
	v_exp_f32_e32 v69, v69
	v_cvt_pk_f16_f32 v161, v66, v67
	v_add_f32_e32 v66, v66, v67
	v_mfma_f32_32x32x16_f16 v[80:95], v[188:191], v[140:143], v[80:95]
	ds_read_b128 v[188:191], v225 offset:18528
	buffer_load_dwordx4 v[208:211], v229, s[4:7], s24 offen
	v_exp_f32_e32 v70, v70
	v_exp_f32_e32 v71, v71
	v_cvt_pk_f16_f32 v162, v68, v69
	v_add_f32_e32 v68, v68, v69
	v_add_f32_e32 v231, v64, v66
	s_waitcnt lgkmcnt(6)
	v_mfma_f32_32x32x16_f16 v[0:15], v[192:195], v[168:171], v[0:15]
	ds_read_b128 v[192:195], v226 offset:9216
	buffer_load_dwordx4 v[212:215], v252, s[4:7], s24 offen
	v_exp_f32_e32 v72, v72
	v_exp_f32_e32 v73, v73
	v_cvt_pk_f16_f32 v163, v70, v71
	v_add_f32_e32 v70, v70, v71
	v_add_f32_e32 v231, v231, v68
	v_mfma_f32_32x32x16_f16 v[16:31], v[196:199], v[168:171], v[16:31]
	ds_read_b128 v[196:199], v226 offset:13824
	v_exp_f32_e32 v74, v74
	v_exp_f32_e32 v75, v75
	v_cvt_pk_f16_f32 v164, v72, v73
	v_add_f32_e32 v72, v72, v73
	v_add_f32_e32 v231, v231, v70
	v_mfma_f32_32x32x16_f16 v[0:15], v[200:203], v[172:175], v[0:15]
	ds_read_b128 v[200:203], v226 offset:9248
	v_exp_f32_e32 v76, v76
	v_exp_f32_e32 v77, v77
	v_cvt_pk_f16_f32 v165, v74, v75
	v_add_f32_e32 v74, v74, v75
	v_add_f32_e32 v231, v231, v72
	v_mfma_f32_32x32x16_f16 v[16:31], v[204:207], v[172:175], v[16:31]
	ds_read_b128 v[204:207], v226 offset:13856
	v_exp_f32_e32 v78, v78
	v_exp_f32_e32 v79, v79
	v_cvt_pk_f16_f32 v166, v76, v77
	v_add_f32_e32 v76, v76, v77
	v_add_f32_e32 v231, v231, v74
	v_cvt_pk_f16_f32 v167, v78, v79
	v_add_f32_e32 v78, v78, v79
	v_add_f32_e32 v231, v231, v76
	v_add_f32_e32 v231, v231, v78
	v_cmp_nge_f32_e32 vcc, s34, v231
	s_cbranch_vccnz .Lovf_a1_10
.Lovfret_a1_10:
	v_add_f32_e32 v232, v232, v231
	s_waitcnt lgkmcnt(4)
	v_mfma_f32_32x32x16_f16 v[64:79], v[176:179], v[128:131], v[96:111]
	ds_read_b128 v[176:179], v225 offset:23040
	s_waitcnt vmcnt(5)
	v_exp_f32_e32 v80, v80
	v_exp_f32_e32 v81, v81
	v_cvt_pk_f16_f32 v216, v216, v217
	v_cvt_pk_f16_f32 v217, v218, v219
	v_mfma_f32_32x32x16_f16 v[64:79], v[180:183], v[132:135], v[64:79]
	ds_read_b128 v[180:183], v225 offset:23072
	v_exp_f32_e32 v82, v82
	v_exp_f32_e32 v83, v83
	v_cvt_pk_f16_f32 v218, v220, v221
	v_cvt_pk_f16_f32 v168, v80, v81
	v_add_f32_e32 v80, v80, v81
	v_cvt_pk_f16_f32 v219, v222, v223
	v_mfma_f32_32x32x16_f16 v[64:79], v[184:187], v[136:139], v[64:79]
	ds_write_b128 v228, v[216:219] offset:18432
	ds_read_b128 v[184:187], v225 offset:23104
	v_exp_f32_e32 v84, v84
	v_exp_f32_e32 v85, v85
	v_cvt_pk_f16_f32 v169, v82, v83
	v_add_f32_e32 v82, v82, v83
	v_mfma_f32_32x32x16_f16 v[64:79], v[188:191], v[140:143], v[64:79]
	ds_read_b128 v[188:191], v225 offset:23136
	buffer_load_dword v216, v230, s[4:7], s25 offen
	buffer_load_dword v217, v245, s[4:7], s25 offen
	v_exp_f32_e32 v86, v86
	v_exp_f32_e32 v87, v87
	v_cvt_pk_f16_f32 v170, v84, v85
	v_add_f32_e32 v84, v84, v85
	v_add_f32_e32 v231, v80, v82
	s_waitcnt lgkmcnt(5)
	v_mfma_f32_32x32x16_f16 v[0:15], v[192:195], v[160:163], v[0:15]
	ds_read_b128 v[192:195], v226 offset:9280
	buffer_load_dword v218, v246, s[4:7], s25 offen
	buffer_load_dword v219, v247, s[4:7], s25 offen
	v_exp_f32_e32 v88, v88
	v_exp_f32_e32 v89, v89
	v_cvt_pk_f16_f32 v171, v86, v87
	v_add_f32_e32 v86, v86, v87
	v_add_f32_e32 v231, v231, v84
	v_mfma_f32_32x32x16_f16 v[16:31], v[196:199], v[160:163], v[16:31]
	ds_read_b128 v[196:199], v226 offset:13888
	buffer_load_dword v220, v248, s[4:7], s25 offen
	buffer_load_dword v221, v249, s[4:7], s25 offen
	v_exp_f32_e32 v90, v90
	v_exp_f32_e32 v91, v91
	v_cvt_pk_f16_f32 v172, v88, v89
	v_add_f32_e32 v88, v88, v89
	v_add_f32_e32 v231, v231, v86
	v_mfma_f32_32x32x16_f16 v[0:15], v[200:203], v[164:167], v[0:15]
	ds_read_b128 v[200:203], v226 offset:9312
	buffer_load_dword v222, v250, s[4:7], s25 offen
	v_exp_f32_e32 v92, v92
	v_exp_f32_e32 v93, v93
	v_cvt_pk_f16_f32 v173, v90, v91
	v_add_f32_e32 v90, v90, v91
	v_add_f32_e32 v231, v231, v88
	v_mfma_f32_32x32x16_f16 v[16:31], v[204:207], v[164:167], v[16:31]
	ds_read_b128 v[204:207], v226 offset:13920
	buffer_load_dword v223, v251, s[4:7], s25 offen
	v_exp_f32_e32 v94, v94
	v_exp_f32_e32 v95, v95
	v_cvt_pk_f16_f32 v174, v92, v93
	v_add_f32_e32 v92, v92, v93
	v_add_f32_e32 v231, v231, v90
	v_cvt_pk_f16_f32 v175, v94, v95
	v_add_f32_e32 v94, v94, v95
	v_add_f32_e32 v231, v231, v92
	v_add_f32_e32 v231, v231, v94
	v_cmp_nge_f32_e32 vcc, s34, v231
	s_cbranch_vccnz .Lovf_a1_11
.Lovfret_a1_11:
	v_add_f32_e32 v232, v232, v231
	s_waitcnt lgkmcnt(6)
	s_barrier
	s_add_u32 s23, s23, 1
	s_waitcnt vmcnt(8)
	v_cmp_ne_u32_e64 s[20:21], 0, v224
	s_add_u32 s31, s23, 1
	s_and_b32 s31, s31, 31
	s_lshl_b32 s31, s31, 8
	s_add_u32 s26, s31, s22
	s_add_u32 s31, s23, 3
	s_and_b32 s31, s31, 31
	s_mul_i32 s31, s31, 0xc0000
	s_add_u32 s24, s31, s18
	s_add_u32 s31, s23, 2
	s_and_b32 s31, s31, 31
	s_mul_i32 s31, s31, 0xc0000
	s_add_u32 s25, s31, s19
	s_cmp_eq_u64 s[20:21], -1
	s_cselect_b32 s34, s37, s38
	s_waitcnt lgkmcnt(4)
	v_mfma_f32_32x32x16_f16 v[80:95], v[176:179], v[128:131], v[96:111]
	ds_read_b128 v[176:179], v225 offset:27648
	s_add_u32 s31, s29, 0xc30000
	buffer_load_dwordx4 v[48:51], v243, s[4:7], s31 offen nt
	s_add_u32 s31, s29, 0xc3c000
	buffer_load_dwordx4 v[52:55], v243, s[4:7], s31 offen nt
	buffer_load_dword v224, v230, s[8:11], s26 offen
	v_exp_f32_e32 v64, v64
	v_exp_f32_e32 v65, v65
	v_cvt_pk_f16_f32 v208, v208, v209
	v_cvt_pk_f16_f32 v209, v210, v211
	v_mfma_f32_32x32x16_f16 v[80:95], v[180:183], v[132:135], v[80:95]
	ds_read_b128 v[180:183], v225 offset:27680
	v_exp_f32_e32 v66, v66
	v_exp_f32_e32 v67, v67
	v_cvt_pk_f16_f32 v212, v212, v213
	v_cvt_pk_f16_f32 v160, v64, v65
	v_add_f32_e32 v64, v64, v65
	v_cvt_pk_f16_f32 v213, v214, v215
	v_mfma_f32_32x32x16_f16 v[80:95], v[184:187], v[136:139], v[80:95]
	ds_write_b64 v227, v[208:209] offset:0
	ds_write_b64 v227, v[212:213] offset:4608
	ds_read_b128 v[184:187], v225 offset:27712
	v_exp_f32_e32 v68, v68
	v_exp_f32_e32 v69, v69
	v_cvt_pk_f16_f32 v161, v66, v67
	v_add_f32_e32 v66, v66, v67
	v_mfma_f32_32x32x16_f16 v[80:95], v[188:191], v[140:143], v[80:95]
	ds_read_b128 v[188:191], v225 offset:27744
	buffer_load_dwordx4 v[208:211], v229, s[4:7], s24 offen
	v_exp_f32_e32 v70, v70
	v_exp_f32_e32 v71, v71
	v_cvt_pk_f16_f32 v162, v68, v69
	v_add_f32_e32 v68, v68, v69
	v_add_f32_e32 v231, v64, v66
	s_waitcnt lgkmcnt(6)
	v_mfma_f32_32x32x16_f16 v[0:15], v[192:195], v[168:171], v[0:15]
	ds_read_b128 v[192:195], v226 offset:18432
	buffer_load_dwordx4 v[212:215], v252, s[4:7], s24 offen
	v_exp_f32_e32 v72, v72
	v_exp_f32_e32 v73, v73
	v_cvt_pk_f16_f32 v163, v70, v71
	v_add_f32_e32 v70, v70, v71
	v_add_f32_e32 v231, v231, v68
	v_mfma_f32_32x32x16_f16 v[16:31], v[196:199], v[168:171], v[16:31]
	ds_read_b128 v[196:199], v226 offset:23040
	v_exp_f32_e32 v74, v74
	v_exp_f32_e32 v75, v75
	v_cvt_pk_f16_f32 v164, v72, v73
	v_add_f32_e32 v72, v72, v73
	v_add_f32_e32 v231, v231, v70
	v_mfma_f32_32x32x16_f16 v[0:15], v[200:203], v[172:175], v[0:15]
	ds_read_b128 v[200:203], v226 offset:18464
	v_exp_f32_e32 v76, v76
	v_exp_f32_e32 v77, v77
	v_cvt_pk_f16_f32 v165, v74, v75
	v_add_f32_e32 v74, v74, v75
	v_add_f32_e32 v231, v231, v72
	v_mfma_f32_32x32x16_f16 v[16:31], v[204:207], v[172:175], v[16:31]
	ds_read_b128 v[204:207], v226 offset:23072
	v_exp_f32_e32 v78, v78
	v_exp_f32_e32 v79, v79
	v_cvt_pk_f16_f32 v166, v76, v77
	v_add_f32_e32 v76, v76, v77
	v_add_f32_e32 v231, v231, v74
	v_cvt_pk_f16_f32 v167, v78, v79
	v_add_f32_e32 v78, v78, v79
	v_add_f32_e32 v231, v231, v76
	v_add_f32_e32 v231, v231, v78
	v_cmp_nge_f32_e32 vcc, s34, v231
	s_cbranch_vccnz .Lovf_a1_20
.Lovfret_a1_20:
	v_add_f32_e32 v232, v232, v231
	s_waitcnt lgkmcnt(4)
	v_mfma_f32_32x32x16_f16 v[64:79], v[176:179], v[128:131], v[96:111]
	ds_read_b128 v[176:179], v225 offset:32256
	s_waitcnt vmcnt(5)
	v_exp_f32_e32 v80, v80
	v_exp_f32_e32 v81, v81
	v_cvt_pk_f16_f32 v216, v216, v217
	v_cvt_pk_f16_f32 v217, v218, v219
	v_mfma_f32_32x32x16_f16 v[64:79], v[180:183], v[132:135], v[64:79]
	ds_read_b128 v[180:183], v225 offset:32288
	v_exp_f32_e32 v82, v82
	v_exp_f32_e32 v83, v83
	v_cvt_pk_f16_f32 v218, v220, v221
	v_cvt_pk_f16_f32 v168, v80, v81
	v_add_f32_e32 v80, v80, v81
	v_cvt_pk_f16_f32 v219, v222, v223
	v_mfma_f32_32x32x16_f16 v[64:79], v[184:187], v[136:139], v[64:79]
	ds_write_b128 v228, v[216:219] offset:27648
	ds_read_b128 v[184:187], v225 offset:32320
	v_exp_f32_e32 v84, v84
	v_exp_f32_e32 v85, v85
	v_cvt_pk_f16_f32 v169, v82, v83
	v_add_f32_e32 v82, v82, v83
	v_mfma_f32_32x32x16_f16 v[64:79], v[188:191], v[140:143], v[64:79]
	ds_read_b128 v[188:191], v225 offset:32352
	buffer_load_dword v216, v230, s[4:7], s25 offen
	buffer_load_dword v217, v245, s[4:7], s25 offen
	v_exp_f32_e32 v86, v86
	v_exp_f32_e32 v87, v87
	v_cvt_pk_f16_f32 v170, v84, v85
	v_add_f32_e32 v84, v84, v85
	v_add_f32_e32 v231, v80, v82
	s_waitcnt lgkmcnt(5)
	v_mfma_f32_32x32x16_f16 v[0:15], v[192:195], v[160:163], v[0:15]
	ds_read_b128 v[192:195], v226 offset:18496
	buffer_load_dword v218, v246, s[4:7], s25 offen
	buffer_load_dword v219, v247, s[4:7], s25 offen
	v_exp_f32_e32 v88, v88
	v_exp_f32_e32 v89, v89
	v_cvt_pk_f16_f32 v171, v86, v87
	v_add_f32_e32 v86, v86, v87
	v_add_f32_e32 v231, v231, v84
	v_mfma_f32_32x32x16_f16 v[16:31], v[196:199], v[160:163], v[16:31]
	ds_read_b128 v[196:199], v226 offset:23104
	buffer_load_dword v220, v248, s[4:7], s25 offen
	buffer_load_dword v221, v249, s[4:7], s25 offen
	v_exp_f32_e32 v90, v90
	v_exp_f32_e32 v91, v91
	v_cvt_pk_f16_f32 v172, v88, v89
	v_add_f32_e32 v88, v88, v89
	v_add_f32_e32 v231, v231, v86
	v_mfma_f32_32x32x16_f16 v[0:15], v[200:203], v[164:167], v[0:15]
	ds_read_b128 v[200:203], v226 offset:18528
	buffer_load_dword v222, v250, s[4:7], s25 offen
	v_exp_f32_e32 v92, v92
	v_exp_f32_e32 v93, v93
	v_cvt_pk_f16_f32 v173, v90, v91
	v_add_f32_e32 v90, v90, v91
	v_add_f32_e32 v231, v231, v88
	v_mfma_f32_32x32x16_f16 v[16:31], v[204:207], v[164:167], v[16:31]
	ds_read_b128 v[204:207], v226 offset:23136
	buffer_load_dword v223, v251, s[4:7], s25 offen
	v_exp_f32_e32 v94, v94
	v_exp_f32_e32 v95, v95
	v_cvt_pk_f16_f32 v174, v92, v93
	v_add_f32_e32 v92, v92, v93
	v_add_f32_e32 v231, v231, v90
	v_cvt_pk_f16_f32 v175, v94, v95
	v_add_f32_e32 v94, v94, v95
	v_add_f32_e32 v231, v231, v92
	v_add_f32_e32 v231, v231, v94
	v_cmp_nge_f32_e32 vcc, s34, v231
	s_cbranch_vccnz .Lovf_a1_21
.Lovfret_a1_21:
	v_add_f32_e32 v232, v232, v231
	s_waitcnt lgkmcnt(6)
	s_barrier
	s_add_u32 s23, s23, 1
	s_waitcnt vmcnt(8)
	v_cmp_ne_u32_e64 s[20:21], 0, v224
	s_add_u32 s31, s23, 1
	s_and_b32 s31, s31, 31
	s_lshl_b32 s31, s31, 8
	s_add_u32 s26, s31, s22
	s_add_u32 s31, s23, 3
	s_and_b32 s31, s31, 31
	s_mul_i32 s31, s31, 0xc0000
	s_add_u32 s24, s31, s18
	s_add_u32 s31, s23, 2
	s_and_b32 s31, s31, 31
	s_mul_i32 s31, s31, 0xc0000
	s_add_u32 s25, s31, s19
	s_cmp_eq_u64 s[20:21], -1
	s_cselect_b32 s34, s37, s38
	s_waitcnt lgkmcnt(4)
	v_mfma_f32_32x32x16_f16 v[80:95], v[176:179], v[128:131], v[96:111]
	ds_read_b128 v[176:179], v225 offset:0
	s_add_u32 s31, s29, 0xc48000
	buffer_load_dwordx4 v[56:59], v243, s[4:7], s31 offen nt
	s_add_u32 s31, s29, 0xc54000
	buffer_load_dwordx4 v[60:63], v243, s[4:7], s31 offen nt
	buffer_load_dword v224, v230, s[8:11], s26 offen
	v_exp_f32_e32 v64, v64
	v_exp_f32_e32 v65, v65
	v_cvt_pk_f16_f32 v208, v208, v209
	v_cvt_pk_f16_f32 v209, v210, v211
	v_mfma_f32_32x32x16_f16 v[80:95], v[180:183], v[132:135], v[80:95]
	ds_read_b128 v[180:183], v225 offset:32
	v_exp_f32_e32 v66, v66
	v_exp_f32_e32 v67, v67
	v_cvt_pk_f16_f32 v212, v212, v213
	v_cvt_pk_f16_f32 v160, v64, v65
	v_add_f32_e32 v64, v64, v65
	v_cvt_pk_f16_f32 v213, v214, v215
	v_mfma_f32_32x32x16_f16 v[80:95], v[184:187], v[136:139], v[80:95]
	ds_write_b64 v227, v[208:209] offset:9216
	ds_write_b64 v227, v[212:213] offset:13824
	ds_read_b128 v[184:187], v225 offset:64
	v_exp_f32_e32 v68, v68
	v_exp_f32_e32 v69, v69
	v_cvt_pk_f16_f32 v161, v66, v67
	v_add_f32_e32 v66, v66, v67
	v_mfma_f32_32x32x16_f16 v[80:95], v[188:191], v[140:143], v[80:95]
	ds_read_b128 v[188:191], v225 offset:96
	buffer_load_dwordx4 v[208:211], v229, s[4:7], s24 offen
	v_exp_f32_e32 v70, v70
	v_exp_f32_e32 v71, v71
	v_cvt_pk_f16_f32 v162, v68, v69
	v_add_f32_e32 v68, v68, v69
	v_add_f32_e32 v231, v64, v66
	s_waitcnt lgkmcnt(6)
	v_mfma_f32_32x32x16_f16 v[0:15], v[192:195], v[168:171], v[0:15]
	ds_read_b128 v[192:195], v226 offset:27648
	buffer_load_dwordx4 v[212:215], v252, s[4:7], s24 offen
	v_exp_f32_e32 v72, v72
	v_exp_f32_e32 v73, v73
	v_cvt_pk_f16_f32 v163, v70, v71
	v_add_f32_e32 v70, v70, v71
	v_add_f32_e32 v231, v231, v68
	v_mfma_f32_32x32x16_f16 v[16:31], v[196:199], v[168:171], v[16:31]
	ds_read_b128 v[196:199], v226 offset:32256
	v_exp_f32_e32 v74, v74
	v_exp_f32_e32 v75, v75
	v_cvt_pk_f16_f32 v164, v72, v73
	v_add_f32_e32 v72, v72, v73
	v_add_f32_e32 v231, v231, v70
	v_mfma_f32_32x32x16_f16 v[0:15], v[200:203], v[172:175], v[0:15]
	ds_read_b128 v[200:203], v226 offset:27680
	v_exp_f32_e32 v76, v76
	v_exp_f32_e32 v77, v77
	v_cvt_pk_f16_f32 v165, v74, v75
	v_add_f32_e32 v74, v74, v75
	v_add_f32_e32 v231, v231, v72
	v_mfma_f32_32x32x16_f16 v[16:31], v[204:207], v[172:175], v[16:31]
	ds_read_b128 v[204:207], v226 offset:32288
	v_exp_f32_e32 v78, v78
	v_exp_f32_e32 v79, v79
	v_cvt_pk_f16_f32 v166, v76, v77
	v_add_f32_e32 v76, v76, v77
	v_add_f32_e32 v231, v231, v74
	v_cvt_pk_f16_f32 v167, v78, v79
	v_add_f32_e32 v78, v78, v79
	v_add_f32_e32 v231, v231, v76
	v_add_f32_e32 v231, v231, v78
	v_cmp_nge_f32_e32 vcc, s34, v231
	s_cbranch_vccnz .Lovf_a1_30
.Lovfret_a1_30:
	v_add_f32_e32 v232, v232, v231
	s_waitcnt lgkmcnt(4)
	v_mfma_f32_32x32x16_f16 v[64:79], v[176:179], v[128:131], v[96:111]
	s_waitcnt vmcnt(5)
	v_exp_f32_e32 v80, v80
	v_exp_f32_e32 v81, v81
	v_cvt_pk_f16_f32 v216, v216, v217
	v_cvt_pk_f16_f32 v217, v218, v219
	v_mfma_f32_32x32x16_f16 v[64:79], v[180:183], v[132:135], v[64:79]
	v_exp_f32_e32 v82, v82
	v_exp_f32_e32 v83, v83
	v_cvt_pk_f16_f32 v218, v220, v221
	v_cvt_pk_f16_f32 v168, v80, v81
	v_add_f32_e32 v80, v80, v81
	v_cvt_pk_f16_f32 v219, v222, v223
	v_mfma_f32_32x32x16_f16 v[64:79], v[184:187], v[136:139], v[64:79]
	ds_write_b128 v228, v[216:219] offset:0
	v_exp_f32_e32 v84, v84
	v_exp_f32_e32 v85, v85
	v_cvt_pk_f16_f32 v169, v82, v83
	v_add_f32_e32 v82, v82, v83
	v_mfma_f32_32x32x16_f16 v[64:79], v[188:191], v[140:143], v[64:79]
	buffer_load_dword v216, v230, s[4:7], s25 offen
	buffer_load_dword v217, v245, s[4:7], s25 offen
	v_exp_f32_e32 v86, v86
	v_exp_f32_e32 v87, v87
	v_cvt_pk_f16_f32 v170, v84, v85
	v_add_f32_e32 v84, v84, v85
	v_add_f32_e32 v231, v80, v82
	s_waitcnt lgkmcnt(1)
	v_mfma_f32_32x32x16_f16 v[0:15], v[192:195], v[160:163], v[0:15]
	ds_read_b128 v[192:195], v226 offset:27712
	buffer_load_dword v218, v246, s[4:7], s25 offen
	buffer_load_dword v219, v247, s[4:7], s25 offen
	v_exp_f32_e32 v88, v88
	v_exp_f32_e32 v89, v89
	v_cvt_pk_f16_f32 v171, v86, v87
	v_add_f32_e32 v86, v86, v87
	v_add_f32_e32 v231, v231, v84
	v_mfma_f32_32x32x16_f16 v[16:31], v[196:199], v[160:163], v[16:31]
	ds_read_b128 v[196:199], v226 offset:32320
	buffer_load_dword v220, v248, s[4:7], s25 offen
	buffer_load_dword v221, v249, s[4:7], s25 offen
	v_exp_f32_e32 v90, v90
	v_exp_f32_e32 v91, v91
	v_cvt_pk_f16_f32 v172, v88, v89
	v_add_f32_e32 v88, v88, v89
	v_add_f32_e32 v231, v231, v86
	v_mfma_f32_32x32x16_f16 v[0:15], v[200:203], v[164:167], v[0:15]
	ds_read_b128 v[200:203], v226 offset:27744
	buffer_load_dword v222, v250, s[4:7], s25 offen
	v_exp_f32_e32 v92, v92
	v_exp_f32_e32 v93, v93
	v_cvt_pk_f16_f32 v173, v90, v91
	v_add_f32_e32 v90, v90, v91
	v_add_f32_e32 v231, v231, v88
	v_mfma_f32_32x32x16_f16 v[16:31], v[204:207], v[164:167], v[16:31]
	ds_read_b128 v[204:207], v226 offset:32352
	buffer_load_dword v223, v251, s[4:7], s25 offen
	v_exp_f32_e32 v94, v94
	v_exp_f32_e32 v95, v95
	v_cvt_pk_f16_f32 v174, v92, v93
	v_add_f32_e32 v92, v92, v93
	v_add_f32_e32 v231, v231, v90
	v_cvt_pk_f16_f32 v175, v94, v95
	v_add_f32_e32 v94, v94, v95
	v_add_f32_e32 v231, v231, v92
	v_add_f32_e32 v231, v231, v94
	v_cmp_nge_f32_e32 vcc, s34, v231
	s_cbranch_vccnz .Lovf_a1_31

.Lbody:
	s_waitcnt lgkmcnt(0)
	v_mfma_f32_32x32x16_f16 v[80:95], v[176:179], v[144:147], v[112:127]
	s_waitcnt vmcnt(8)
	v_cmp_ne_u32_e64 s[20:21], 0, v224
	s_add_u32 s31, s23, 1
	s_and_b32 s31, s31, 31
	s_lshl_b32 s31, s31, 8
	s_add_u32 s26, s31, s22
	s_add_u32 s31, s23, 3
	s_and_b32 s31, s31, 31
	s_mul_i32 s31, s31, 0xc0000
	s_add_u32 s24, s31, s18
	s_add_u32 s31, s23, 2
	s_and_b32 s31, s31, 31
	s_mul_i32 s31, s31, 0xc0000
	s_add_u32 s25, s31, s19
	s_cmp_eq_u64 s[20:21], -1
	s_cselect_b32 s34, s37, s38
	ds_read_b128 v[176:179], v225 offset:4608
	buffer_load_dword v224, v230, s[8:11], s26 offen
	v_exp_f32_e32 v64, v64
	v_exp_f32_e32 v65, v65
	v_cvt_pk_f16_f32 v208, v208, v209
	v_cvt_pk_f16_f32 v209, v210, v211
	v_mfma_f32_32x32x16_f16 v[80:95], v[180:183], v[148:151], v[80:95]
	ds_read_b128 v[180:183], v225 offset:4640
	v_exp_f32_e32 v66, v66
	v_exp_f32_e32 v67, v67
	v_cvt_pk_f16_f32 v212, v212, v213
	v_cvt_pk_f16_f32 v160, v64, v65
	v_add_f32_e32 v64, v64, v65
	v_cvt_pk_f16_f32 v213, v214, v215
	v_mfma_f32_32x32x16_f16 v[80:95], v[184:187], v[152:155], v[80:95]
	ds_write_b64 v227, v[208:209] offset:18432
	ds_write_b64 v227, v[212:213] offset:23040
	ds_read_b128 v[184:187], v225 offset:4672
	v_exp_f32_e32 v68, v68
	v_exp_f32_e32 v69, v69
	v_cvt_pk_f16_f32 v161, v66, v67
	v_add_f32_e32 v66, v66, v67
	v_mfma_f32_32x32x16_f16 v[80:95], v[188:191], v[156:159], v[80:95]
	ds_read_b128 v[188:191], v225 offset:4704
	v_exp_f32_e32 v70, v70
	v_exp_f32_e32 v71, v71
	v_cvt_pk_f16_f32 v162, v68, v69
	v_add_f32_e32 v68, v68, v69
	v_add_f32_e32 v231, v64, v66
	v_mfma_f32_32x32x16_f16 v[32:47], v[192:195], v[168:171], v[32:47]
	ds_read_b128 v[192:195], v226 offset:0
	v_exp_f32_e32 v72, v72
	v_exp_f32_e32 v73, v73
	v_cvt_pk_f16_f32 v163, v70, v71
	v_add_f32_e32 v70, v70, v71
	v_add_f32_e32 v231, v231, v68
	v_mfma_f32_32x32x16_f16 v[48:63], v[196:199], v[168:171], v[48:63]
	ds_read_b128 v[196:199], v226 offset:4608
	v_exp_f32_e32 v74, v74
	v_exp_f32_e32 v75, v75
	v_cvt_pk_f16_f32 v164, v72, v73
	v_add_f32_e32 v72, v72, v73
	v_add_f32_e32 v231, v231, v70
	v_mfma_f32_32x32x16_f16 v[32:47], v[200:203], v[172:175], v[32:47]
	ds_read_b128 v[200:203], v226 offset:32
	v_exp_f32_e32 v76, v76
	v_exp_f32_e32 v77, v77
	v_cvt_pk_f16_f32 v165, v74, v75
	v_add_f32_e32 v74, v74, v75
	v_add_f32_e32 v231, v231, v72
	v_mfma_f32_32x32x16_f16 v[48:63], v[204:207], v[172:175], v[48:63]
	ds_read_b128 v[204:207], v226 offset:4640
	v_exp_f32_e32 v78, v78
	v_exp_f32_e32 v79, v79
	v_cvt_pk_f16_f32 v166, v76, v77
	v_add_f32_e32 v76, v76, v77
	v_add_f32_e32 v231, v231, v74
	v_cvt_pk_f16_f32 v167, v78, v79
	v_add_f32_e32 v78, v78, v79
	v_add_f32_e32 v231, v231, v76
	v_add_f32_e32 v231, v231, v78
	v_cmp_nge_f32_e32 vcc, s34, v231
	s_cbranch_vccnz .Lovf_a00
.Lovfret_a00:
	v_add_f32_e32 v232, v232, v231
	s_waitcnt lgkmcnt(4)
	v_mfma_f32_32x32x16_f16 v[64:79], v[176:179], v[128:131], v[96:111]
	v_exp_f32_e32 v80, v80
	v_exp_f32_e32 v81, v81
	v_mfma_f32_32x32x16_f16 v[64:79], v[180:183], v[132:135], v[64:79]
	buffer_load_dwordx4 v[208:211], v229, s[4:7], s24 offen
	v_exp_f32_e32 v82, v82
	v_exp_f32_e32 v83, v83
	v_cvt_pk_f16_f32 v168, v80, v81
	v_add_f32_e32 v80, v80, v81
	v_mfma_f32_32x32x16_f16 v[64:79], v[184:187], v[136:139], v[64:79]
	buffer_load_dwordx4 v[212:215], v252, s[4:7], s24 offen
	v_exp_f32_e32 v84, v84
	v_exp_f32_e32 v85, v85
	v_cvt_pk_f16_f32 v169, v82, v83
	v_add_f32_e32 v82, v82, v83
	v_mfma_f32_32x32x16_f16 v[64:79], v[188:191], v[140:143], v[64:79]
	v_exp_f32_e32 v86, v86
	v_exp_f32_e32 v87, v87
	v_cvt_pk_f16_f32 v170, v84, v85
	v_add_f32_e32 v84, v84, v85
	v_add_f32_e32 v231, v80, v82
	s_waitcnt lgkmcnt(0)
	v_mfma_f32_32x32x16_f16 v[0:15], v[192:195], v[160:163], v[0:15]
	v_exp_f32_e32 v88, v88
	v_exp_f32_e32 v89, v89
	v_cvt_pk_f16_f32 v171, v86, v87
	v_add_f32_e32 v86, v86, v87
	v_add_f32_e32 v231, v231, v84
	v_mfma_f32_32x32x16_f16 v[16:31], v[196:199], v[160:163], v[16:31]
	v_exp_f32_e32 v90, v90
	v_exp_f32_e32 v91, v91
	v_cvt_pk_f16_f32 v172, v88, v89
	v_add_f32_e32 v88, v88, v89
	v_add_f32_e32 v231, v231, v86
	v_mfma_f32_32x32x16_f16 v[0:15], v[200:203], v[164:167], v[0:15]
	v_exp_f32_e32 v92, v92
	v_exp_f32_e32 v93, v93
	v_cvt_pk_f16_f32 v173, v90, v91
	v_add_f32_e32 v90, v90, v91
	v_add_f32_e32 v231, v231, v88
	v_mfma_f32_32x32x16_f16 v[16:31], v[204:207], v[164:167], v[16:31]
	v_exp_f32_e32 v94, v94
	v_exp_f32_e32 v95, v95
	v_cvt_pk_f16_f32 v174, v92, v93
	v_add_f32_e32 v92, v92, v93
	v_add_f32_e32 v231, v231, v90
	v_cvt_pk_f16_f32 v175, v94, v95
	v_add_f32_e32 v94, v94, v95
	v_add_f32_e32 v231, v231, v92
	v_add_f32_e32 v231, v231, v94
	v_cmp_nge_f32_e32 vcc, s34, v231
	s_cbranch_vccnz .Lovf_b00
.Lovfret_b00:
	v_add_f32_e32 v233, v233, v231
	s_waitcnt lgkmcnt(0)
	v_mfma_f32_32x32x16_f16 v[80:95], v[176:179], v[144:147], v[112:127]
	ds_read_b128 v[176:179], v225 offset:9216
	s_waitcnt vmcnt(3)
	v_exp_f32_e32 v64, v64
	v_exp_f32_e32 v65, v65
	v_cvt_pk_f16_f32 v216, v216, v217
	v_cvt_pk_f16_f32 v217, v218, v219
	v_mfma_f32_32x32x16_f16 v[80:95], v[180:183], v[148:151], v[80:95]
	ds_read_b128 v[180:183], v225 offset:9248
	v_exp_f32_e32 v66, v66
	v_exp_f32_e32 v67, v67
	v_cvt_pk_f16_f32 v218, v220, v221
	v_cvt_pk_f16_f32 v160, v64, v65
	v_add_f32_e32 v64, v64, v65
	v_cvt_pk_f16_f32 v219, v222, v223
	v_mfma_f32_32x32x16_f16 v[80:95], v[184:187], v[152:155], v[80:95]
	ds_write_b128 v228, v[216:219] offset:9216
	ds_read_b128 v[184:187], v225 offset:9280
	v_exp_f32_e32 v68, v68
	v_exp_f32_e32 v69, v69
	v_cvt_pk_f16_f32 v161, v66, v67
	v_add_f32_e32 v66, v66, v67
	v_mfma_f32_32x32x16_f16 v[80:95], v[188:191], v[156:159], v[80:95]
	ds_read_b128 v[188:191], v225 offset:9312
	v_exp_f32_e32 v70, v70
	v_exp_f32_e32 v71, v71
	v_cvt_pk_f16_f32 v162, v68, v69
	v_add_f32_e32 v68, v68, v69
	v_add_f32_e32 v231, v64, v66
	v_mfma_f32_32x32x16_f16 v[32:47], v[192:195], v[168:171], v[32:47]
	ds_read_b128 v[192:195], v226 offset:64
	v_exp_f32_e32 v72, v72
	v_exp_f32_e32 v73, v73
	v_cvt_pk_f16_f32 v163, v70, v71
	v_add_f32_e32 v70, v70, v71
	v_add_f32_e32 v231, v231, v68
	v_mfma_f32_32x32x16_f16 v[48:63], v[196:199], v[168:171], v[48:63]
	ds_read_b128 v[196:199], v226 offset:4672
	v_exp_f32_e32 v74, v74
	v_exp_f32_e32 v75, v75
	v_cvt_pk_f16_f32 v164, v72, v73
	v_add_f32_e32 v72, v72, v73
	v_add_f32_e32 v231, v231, v70
	v_mfma_f32_32x32x16_f16 v[32:47], v[200:203], v[172:175], v[32:47]
	ds_read_b128 v[200:203], v226 offset:96
	v_exp_f32_e32 v76, v76
	v_exp_f32_e32 v77, v77
	v_cvt_pk_f16_f32 v165, v74, v75
	v_add_f32_e32 v74, v74, v75
	v_add_f32_e32 v231, v231, v72
	v_mfma_f32_32x32x16_f16 v[48:63], v[204:207], v[172:175], v[48:63]
	ds_read_b128 v[204:207], v226 offset:4704
	v_exp_f32_e32 v78, v78
	v_exp_f32_e32 v79, v79
	v_cvt_pk_f16_f32 v166, v76, v77
	v_add_f32_e32 v76, v76, v77
	v_add_f32_e32 v231, v231, v74
	v_cvt_pk_f16_f32 v167, v78, v79
	v_add_f32_e32 v78, v78, v79
	v_add_f32_e32 v231, v231, v76
	v_add_f32_e32 v231, v231, v78
	v_cmp_nge_f32_e32 vcc, s34, v231
	s_cbranch_vccnz .Lovf_a01
.Lovfret_a01:
	v_add_f32_e32 v232, v232, v231
	s_waitcnt lgkmcnt(4)
	v_mfma_f32_32x32x16_f16 v[64:79], v[176:179], v[128:131], v[96:111]
	buffer_load_dword v216, v230, s[4:7], s25 offen
	v_exp_f32_e32 v80, v80
	v_exp_f32_e32 v81, v81
	v_mfma_f32_32x32x16_f16 v[64:79], v[180:183], v[132:135], v[64:79]
	buffer_load_dword v217, v245, s[4:7], s25 offen
	v_exp_f32_e32 v82, v82
	v_exp_f32_e32 v83, v83
	v_cvt_pk_f16_f32 v168, v80, v81
	v_add_f32_e32 v80, v80, v81
	v_mfma_f32_32x32x16_f16 v[64:79], v[184:187], v[136:139], v[64:79]
	buffer_load_dword v218, v246, s[4:7], s25 offen
	v_exp_f32_e32 v84, v84
	v_exp_f32_e32 v85, v85
	v_cvt_pk_f16_f32 v169, v82, v83
	v_add_f32_e32 v82, v82, v83
	v_mfma_f32_32x32x16_f16 v[64:79], v[188:191], v[140:143], v[64:79]
	buffer_load_dword v219, v247, s[4:7], s25 offen
	v_exp_f32_e32 v86, v86
	v_exp_f32_e32 v87, v87
	v_cvt_pk_f16_f32 v170, v84, v85
	v_add_f32_e32 v84, v84, v85
	v_add_f32_e32 v231, v80, v82
	s_waitcnt lgkmcnt(0)
	v_mfma_f32_32x32x16_f16 v[0:15], v[192:195], v[160:163], v[0:15]
	buffer_load_dword v220, v248, s[4:7], s25 offen
	v_exp_f32_e32 v88, v88
	v_exp_f32_e32 v89, v89
	v_cvt_pk_f16_f32 v171, v86, v87
	v_add_f32_e32 v86, v86, v87
	v_add_f32_e32 v231, v231, v84
	v_mfma_f32_32x32x16_f16 v[16:31], v[196:199], v[160:163], v[16:31]
	buffer_load_dword v221, v249, s[4:7], s25 offen
	v_exp_f32_e32 v90, v90
	v_exp_f32_e32 v91, v91
	v_cvt_pk_f16_f32 v172, v88, v89
	v_add_f32_e32 v88, v88, v89
	v_add_f32_e32 v231, v231, v86
	v_mfma_f32_32x32x16_f16 v[0:15], v[200:203], v[164:167], v[0:15]
	buffer_load_dword v222, v250, s[4:7], s25 offen
	v_exp_f32_e32 v92, v92
	v_exp_f32_e32 v93, v93
	v_cvt_pk_f16_f32 v173, v90, v91
	v_add_f32_e32 v90, v90, v91
	v_add_f32_e32 v231, v231, v88
	v_mfma_f32_32x32x16_f16 v[16:31], v[204:207], v[164:167], v[16:31]
	buffer_load_dword v223, v251, s[4:7], s25 offen
	v_exp_f32_e32 v94, v94
	v_exp_f32_e32 v95, v95
	v_cvt_pk_f16_f32 v174, v92, v93
	v_add_f32_e32 v92, v92, v93
	v_add_f32_e32 v231, v231, v90
	v_cvt_pk_f16_f32 v175, v94, v95
	v_add_f32_e32 v94, v94, v95
	v_add_f32_e32 v231, v231, v92
	v_add_f32_e32 v231, v231, v94
	v_cmp_nge_f32_e32 vcc, s34, v231
	s_cbranch_vccnz .Lovf_b01
.Lovfret_b01:
	v_add_f32_e32 v233, v233, v231
	s_waitcnt lgkmcnt(6)
	s_barrier
	s_add_u32 s23, s23, 1
	s_waitcnt lgkmcnt(0)
	v_mfma_f32_32x32x16_f16 v[80:95], v[176:179], v[144:147], v[112:127]
	s_waitcnt vmcnt(8)
	v_cmp_ne_u32_e64 s[20:21], 0, v224
	s_add_u32 s31, s23, 1
	s_and_b32 s31, s31, 31
	s_lshl_b32 s31, s31, 8
	s_add_u32 s26, s31, s22
	s_add_u32 s31, s23, 3
	s_and_b32 s31, s31, 31
	s_mul_i32 s31, s31, 0xc0000
	s_add_u32 s24, s31, s18
	s_add_u32 s31, s23, 2
	s_and_b32 s31, s31, 31
	s_mul_i32 s31, s31, 0xc0000
	s_add_u32 s25, s31, s19
	s_cmp_eq_u64 s[20:21], -1
	s_cselect_b32 s34, s37, s38
	ds_read_b128 v[176:179], v225 offset:13824
	buffer_load_dword v224, v230, s[8:11], s26 offen
	v_exp_f32_e32 v64, v64
	v_exp_f32_e32 v65, v65
	v_cvt_pk_f16_f32 v208, v208, v209
	v_cvt_pk_f16_f32 v209, v210, v211
	v_mfma_f32_32x32x16_f16 v[80:95], v[180:183], v[148:151], v[80:95]
	ds_read_b128 v[180:183], v225 offset:13856
	v_exp_f32_e32 v66, v66
	v_exp_f32_e32 v67, v67
	v_cvt_pk_f16_f32 v212, v212, v213
	v_cvt_pk_f16_f32 v160, v64, v65
	v_add_f32_e32 v64, v64, v65
	v_cvt_pk_f16_f32 v213, v214, v215
	v_mfma_f32_32x32x16_f16 v[80:95], v[184:187], v[152:155], v[80:95]
	ds_write_b64 v227, v[208:209] offset:27648
	ds_write_b64 v227, v[212:213] offset:32256
	ds_read_b128 v[184:187], v225 offset:13888
	v_exp_f32_e32 v68, v68
	v_exp_f32_e32 v69, v69
	v_cvt_pk_f16_f32 v161, v66, v67
	v_add_f32_e32 v66, v66, v67
	v_mfma_f32_32x32x16_f16 v[80:95], v[188:191], v[156:159], v[80:95]
	ds_read_b128 v[188:191], v225 offset:13920
	v_exp_f32_e32 v70, v70
	v_exp_f32_e32 v71, v71
	v_cvt_pk_f16_f32 v162, v68, v69
	v_add_f32_e32 v68, v68, v69
	v_add_f32_e32 v231, v64, v66
	v_mfma_f32_32x32x16_f16 v[32:47], v[192:195], v[168:171], v[32:47]
	ds_read_b128 v[192:195], v226 offset:9216
	v_exp_f32_e32 v72, v72
	v_exp_f32_e32 v73, v73
	v_cvt_pk_f16_f32 v163, v70, v71
	v_add_f32_e32 v70, v70, v71
	v_add_f32_e32 v231, v231, v68
	v_mfma_f32_32x32x16_f16 v[48:63], v[196:199], v[168:171], v[48:63]
	ds_read_b128 v[196:199], v226 offset:13824
	v_exp_f32_e32 v74, v74
	v_exp_f32_e32 v75, v75
	v_cvt_pk_f16_f32 v164, v72, v73
	v_add_f32_e32 v72, v72, v73
	v_add_f32_e32 v231, v231, v70
	v_mfma_f32_32x32x16_f16 v[32:47], v[200:203], v[172:175], v[32:47]
	ds_read_b128 v[200:203], v226 offset:9248
	v_exp_f32_e32 v76, v76
	v_exp_f32_e32 v77, v77
	v_cvt_pk_f16_f32 v165, v74, v75
	v_add_f32_e32 v74, v74, v75
	v_add_f32_e32 v231, v231, v72
	v_mfma_f32_32x32x16_f16 v[48:63], v[204:207], v[172:175], v[48:63]
	ds_read_b128 v[204:207], v226 offset:13856
	v_exp_f32_e32 v78, v78
	v_exp_f32_e32 v79, v79
	v_cvt_pk_f16_f32 v166, v76, v77
	v_add_f32_e32 v76, v76, v77
	v_add_f32_e32 v231, v231, v74
	v_cvt_pk_f16_f32 v167, v78, v79
	v_add_f32_e32 v78, v78, v79
	v_add_f32_e32 v231, v231, v76
	v_add_f32_e32 v231, v231, v78
	v_cmp_nge_f32_e32 vcc, s34, v231
	s_cbranch_vccnz .Lovf_a10

.Lovfret_b10:
	v_add_f32_e32 v233, v233, v231
	s_waitcnt lgkmcnt(0)
	v_mfma_f32_32x32x16_f16 v[80:95], v[176:179], v[144:147], v[112:127]
	ds_read_b128 v[176:179], v225 offset:18432
	s_waitcnt vmcnt(3)
	v_exp_f32_e32 v64, v64
	v_exp_f32_e32 v65, v65
	v_cvt_pk_f16_f32 v216, v216, v217
	v_cvt_pk_f16_f32 v217, v218, v219
	v_mfma_f32_32x32x16_f16 v[80:95], v[180:183], v[148:151], v[80:95]
	ds_read_b128 v[180:183], v225 offset:18464
	v_exp_f32_e32 v66, v66
	v_exp_f32_e32 v67, v67
	v_cvt_pk_f16_f32 v218, v220, v221
	v_cvt_pk_f16_f32 v160, v64, v65
	v_add_f32_e32 v64, v64, v65
	v_cvt_pk_f16_f32 v219, v222, v223
	v_mfma_f32_32x32x16_f16 v[80:95], v[184:187], v[152:155], v[80:95]
	ds_write_b128 v228, v[216:219] offset:18432
	ds_read_b128 v[184:187], v225 offset:18496
	v_exp_f32_e32 v68, v68
	v_exp_f32_e32 v69, v69
	v_cvt_pk_f16_f32 v161, v66, v67
	v_add_f32_e32 v66, v66, v67
	v_mfma_f32_32x32x16_f16 v[80:95], v[188:191], v[156:159], v[80:95]
	ds_read_b128 v[188:191], v225 offset:18528
	v_exp_f32_e32 v70, v70
	v_exp_f32_e32 v71, v71
	v_cvt_pk_f16_f32 v162, v68, v69
	v_add_f32_e32 v68, v68, v69
	v_add_f32_e32 v231, v64, v66
	v_mfma_f32_32x32x16_f16 v[32:47], v[192:195], v[168:171], v[32:47]
	ds_read_b128 v[192:195], v226 offset:9280
	v_exp_f32_e32 v72, v72
	v_exp_f32_e32 v73, v73
	v_cvt_pk_f16_f32 v163, v70, v71
	v_add_f32_e32 v70, v70, v71
	v_add_f32_e32 v231, v231, v68
	v_mfma_f32_32x32x16_f16 v[48:63], v[196:199], v[168:171], v[48:63]
	ds_read_b128 v[196:199], v226 offset:13888
	v_exp_f32_e32 v74, v74
	v_exp_f32_e32 v75, v75
	v_cvt_pk_f16_f32 v164, v72, v73
	v_add_f32_e32 v72, v72, v73
	v_add_f32_e32 v231, v231, v70
	v_mfma_f32_32x32x16_f16 v[32:47], v[200:203], v[172:175], v[32:47]
	ds_read_b128 v[200:203], v226 offset:9312
	v_exp_f32_e32 v76, v76
	v_exp_f32_e32 v77, v77
	v_cvt_pk_f16_f32 v165, v74, v75
	v_add_f32_e32 v74, v74, v75
	v_add_f32_e32 v231, v231, v72
	v_mfma_f32_32x32x16_f16 v[48:63], v[204:207], v[172:175], v[48:63]
	ds_read_b128 v[204:207], v226 offset:13920
	v_exp_f32_e32 v78, v78
	v_exp_f32_e32 v79, v79
	v_cvt_pk_f16_f32 v166, v76, v77
	v_add_f32_e32 v76, v76, v77
	v_add_f32_e32 v231, v231, v74
	v_cvt_pk_f16_f32 v167, v78, v79
	v_add_f32_e32 v78, v78, v79
	v_add_f32_e32 v231, v231, v76
	v_add_f32_e32 v231, v231, v78
	v_cmp_nge_f32_e32 vcc, s34, v231
	s_cbranch_vccnz .Lovf_a11

.Lovfret_b11:
	v_add_f32_e32 v233, v233, v231
	s_waitcnt lgkmcnt(6)
	s_barrier
	s_add_u32 s23, s23, 1
	s_waitcnt lgkmcnt(0)
	v_mfma_f32_32x32x16_f16 v[80:95], v[176:179], v[144:147], v[112:127]
	s_waitcnt vmcnt(8)
	v_cmp_ne_u32_e64 s[20:21], 0, v224
	s_add_u32 s31, s23, 1
	s_and_b32 s31, s31, 31
	s_lshl_b32 s31, s31, 8
	s_add_u32 s26, s31, s22
	s_add_u32 s31, s23, 3
	s_and_b32 s31, s31, 31
	s_mul_i32 s31, s31, 0xc0000
	s_add_u32 s24, s31, s18
	s_add_u32 s31, s23, 2
	s_and_b32 s31, s31, 31
	s_mul_i32 s31, s31, 0xc0000
	s_add_u32 s25, s31, s19
	s_cmp_eq_u64 s[20:21], -1
	s_cselect_b32 s34, s37, s38
	ds_read_b128 v[176:179], v225 offset:23040
	buffer_load_dword v224, v230, s[8:11], s26 offen
	v_exp_f32_e32 v64, v64
	v_exp_f32_e32 v65, v65
	v_cvt_pk_f16_f32 v208, v208, v209
	v_cvt_pk_f16_f32 v209, v210, v211
	v_mfma_f32_32x32x16_f16 v[80:95], v[180:183], v[148:151], v[80:95]
	ds_read_b128 v[180:183], v225 offset:23072
	v_exp_f32_e32 v66, v66
	v_exp_f32_e32 v67, v67
	v_cvt_pk_f16_f32 v212, v212, v213
	v_cvt_pk_f16_f32 v160, v64, v65
	v_add_f32_e32 v64, v64, v65
	v_cvt_pk_f16_f32 v213, v214, v215
	v_mfma_f32_32x32x16_f16 v[80:95], v[184:187], v[152:155], v[80:95]
	ds_write_b64 v227, v[208:209] offset:0
	ds_write_b64 v227, v[212:213] offset:4608
	ds_read_b128 v[184:187], v225 offset:23104
	v_exp_f32_e32 v68, v68
	v_exp_f32_e32 v69, v69
	v_cvt_pk_f16_f32 v161, v66, v67
	v_add_f32_e32 v66, v66, v67
	v_mfma_f32_32x32x16_f16 v[80:95], v[188:191], v[156:159], v[80:95]
	ds_read_b128 v[188:191], v225 offset:23136
	v_exp_f32_e32 v70, v70
	v_exp_f32_e32 v71, v71
	v_cvt_pk_f16_f32 v162, v68, v69
	v_add_f32_e32 v68, v68, v69
	v_add_f32_e32 v231, v64, v66
	v_mfma_f32_32x32x16_f16 v[32:47], v[192:195], v[168:171], v[32:47]
	ds_read_b128 v[192:195], v226 offset:18432
	v_exp_f32_e32 v72, v72
	v_exp_f32_e32 v73, v73
	v_cvt_pk_f16_f32 v163, v70, v71
	v_add_f32_e32 v70, v70, v71
	v_add_f32_e32 v231, v231, v68
	v_mfma_f32_32x32x16_f16 v[48:63], v[196:199], v[168:171], v[48:63]
	ds_read_b128 v[196:199], v226 offset:23040
	v_exp_f32_e32 v74, v74
	v_exp_f32_e32 v75, v75
	v_cvt_pk_f16_f32 v164, v72, v73
	v_add_f32_e32 v72, v72, v73
	v_add_f32_e32 v231, v231, v70
	v_mfma_f32_32x32x16_f16 v[32:47], v[200:203], v[172:175], v[32:47]
	ds_read_b128 v[200:203], v226 offset:18464
	v_exp_f32_e32 v76, v76
	v_exp_f32_e32 v77, v77
	v_cvt_pk_f16_f32 v165, v74, v75
	v_add_f32_e32 v74, v74, v75
	v_add_f32_e32 v231, v231, v72
	v_mfma_f32_32x32x16_f16 v[48:63], v[204:207], v[172:175], v[48:63]
	ds_read_b128 v[204:207], v226 offset:23072
	v_exp_f32_e32 v78, v78
	v_exp_f32_e32 v79, v79
	v_cvt_pk_f16_f32 v166, v76, v77
	v_add_f32_e32 v76, v76, v77
	v_add_f32_e32 v231, v231, v74
	v_cvt_pk_f16_f32 v167, v78, v79
	v_add_f32_e32 v78, v78, v79
	v_add_f32_e32 v231, v231, v76
	v_add_f32_e32 v231, v231, v78
	v_cmp_nge_f32_e32 vcc, s34, v231
	s_cbranch_vccnz .Lovf_a20

.Lovfret_b20:
	v_add_f32_e32 v233, v233, v231
	s_waitcnt lgkmcnt(0)
	v_mfma_f32_32x32x16_f16 v[80:95], v[176:179], v[144:147], v[112:127]
	ds_read_b128 v[176:179], v225 offset:27648
	s_waitcnt vmcnt(3)
	v_exp_f32_e32 v64, v64
	v_exp_f32_e32 v65, v65
	v_cvt_pk_f16_f32 v216, v216, v217
	v_cvt_pk_f16_f32 v217, v218, v219
	v_mfma_f32_32x32x16_f16 v[80:95], v[180:183], v[148:151], v[80:95]
	ds_read_b128 v[180:183], v225 offset:27680
	v_exp_f32_e32 v66, v66
	v_exp_f32_e32 v67, v67
	v_cvt_pk_f16_f32 v218, v220, v221
	v_cvt_pk_f16_f32 v160, v64, v65
	v_add_f32_e32 v64, v64, v65
	v_cvt_pk_f16_f32 v219, v222, v223
	v_mfma_f32_32x32x16_f16 v[80:95], v[184:187], v[152:155], v[80:95]
	ds_write_b128 v228, v[216:219] offset:27648
	ds_read_b128 v[184:187], v225 offset:27712
	v_exp_f32_e32 v68, v68
	v_exp_f32_e32 v69, v69
	v_cvt_pk_f16_f32 v161, v66, v67
	v_add_f32_e32 v66, v66, v67
	v_mfma_f32_32x32x16_f16 v[80:95], v[188:191], v[156:159], v[80:95]
	ds_read_b128 v[188:191], v225 offset:27744
	v_exp_f32_e32 v70, v70
	v_exp_f32_e32 v71, v71
	v_cvt_pk_f16_f32 v162, v68, v69
	v_add_f32_e32 v68, v68, v69
	v_add_f32_e32 v231, v64, v66
	v_mfma_f32_32x32x16_f16 v[32:47], v[192:195], v[168:171], v[32:47]
	ds_read_b128 v[192:195], v226 offset:18496
	v_exp_f32_e32 v72, v72
	v_exp_f32_e32 v73, v73
	v_cvt_pk_f16_f32 v163, v70, v71
	v_add_f32_e32 v70, v70, v71
	v_add_f32_e32 v231, v231, v68
	v_mfma_f32_32x32x16_f16 v[48:63], v[196:199], v[168:171], v[48:63]
	ds_read_b128 v[196:199], v226 offset:23104
	v_exp_f32_e32 v74, v74
	v_exp_f32_e32 v75, v75
	v_cvt_pk_f16_f32 v164, v72, v73
	v_add_f32_e32 v72, v72, v73
	v_add_f32_e32 v231, v231, v70
	v_mfma_f32_32x32x16_f16 v[32:47], v[200:203], v[172:175], v[32:47]
	ds_read_b128 v[200:203], v226 offset:18528
	v_exp_f32_e32 v76, v76
	v_exp_f32_e32 v77, v77
	v_cvt_pk_f16_f32 v165, v74, v75
	v_add_f32_e32 v74, v74, v75
	v_add_f32_e32 v231, v231, v72
	v_mfma_f32_32x32x16_f16 v[48:63], v[204:207], v[172:175], v[48:63]
	ds_read_b128 v[204:207], v226 offset:23136
	v_exp_f32_e32 v78, v78
	v_exp_f32_e32 v79, v79
	v_cvt_pk_f16_f32 v166, v76, v77
	v_add_f32_e32 v76, v76, v77
	v_add_f32_e32 v231, v231, v74
	v_cvt_pk_f16_f32 v167, v78, v79
	v_add_f32_e32 v78, v78, v79
	v_add_f32_e32 v231, v231, v76
	v_add_f32_e32 v231, v231, v78
	v_cmp_nge_f32_e32 vcc, s34, v231
	s_cbranch_vccnz .Lovf_a21

.Lovfret_b21:
	v_add_f32_e32 v233, v233, v231
	s_waitcnt lgkmcnt(6)
	s_barrier
	s_add_u32 s23, s23, 1
	s_waitcnt lgkmcnt(0)
	v_mfma_f32_32x32x16_f16 v[80:95], v[176:179], v[144:147], v[112:127]
	s_waitcnt vmcnt(8)
	v_cmp_ne_u32_e64 s[20:21], 0, v224
	s_add_u32 s31, s23, 1
	s_and_b32 s31, s31, 31
	s_lshl_b32 s31, s31, 8
	s_add_u32 s26, s31, s22
	s_add_u32 s31, s23, 3
	s_and_b32 s31, s31, 31
	s_mul_i32 s31, s31, 0xc0000
	s_add_u32 s24, s31, s18
	s_add_u32 s31, s23, 2
	s_and_b32 s31, s31, 31
	s_mul_i32 s31, s31, 0xc0000
	s_add_u32 s25, s31, s19
	s_cmp_eq_u64 s[20:21], -1
	s_cselect_b32 s34, s37, s38
	ds_read_b128 v[176:179], v225 offset:32256
	buffer_load_dword v224, v230, s[8:11], s26 offen
	v_exp_f32_e32 v64, v64
	v_exp_f32_e32 v65, v65
	v_cvt_pk_f16_f32 v208, v208, v209
	v_cvt_pk_f16_f32 v209, v210, v211
	v_mfma_f32_32x32x16_f16 v[80:95], v[180:183], v[148:151], v[80:95]
	ds_read_b128 v[180:183], v225 offset:32288
	v_exp_f32_e32 v66, v66
	v_exp_f32_e32 v67, v67
	v_cvt_pk_f16_f32 v212, v212, v213
	v_cvt_pk_f16_f32 v160, v64, v65
	v_add_f32_e32 v64, v64, v65
	v_cvt_pk_f16_f32 v213, v214, v215
	v_mfma_f32_32x32x16_f16 v[80:95], v[184:187], v[152:155], v[80:95]
	ds_write_b64 v227, v[208:209] offset:9216
	ds_write_b64 v227, v[212:213] offset:13824
	ds_read_b128 v[184:187], v225 offset:32320
	v_exp_f32_e32 v68, v68
	v_exp_f32_e32 v69, v69
	v_cvt_pk_f16_f32 v161, v66, v67
	v_add_f32_e32 v66, v66, v67
	v_mfma_f32_32x32x16_f16 v[80:95], v[188:191], v[156:159], v[80:95]
	ds_read_b128 v[188:191], v225 offset:32352
	v_exp_f32_e32 v70, v70
	v_exp_f32_e32 v71, v71
	v_cvt_pk_f16_f32 v162, v68, v69
	v_add_f32_e32 v68, v68, v69
	v_add_f32_e32 v231, v64, v66
	v_mfma_f32_32x32x16_f16 v[32:47], v[192:195], v[168:171], v[32:47]
	ds_read_b128 v[192:195], v226 offset:27648
	v_exp_f32_e32 v72, v72
	v_exp_f32_e32 v73, v73
	v_cvt_pk_f16_f32 v163, v70, v71
	v_add_f32_e32 v70, v70, v71
	v_add_f32_e32 v231, v231, v68
	v_mfma_f32_32x32x16_f16 v[48:63], v[196:199], v[168:171], v[48:63]
	ds_read_b128 v[196:199], v226 offset:32256
	v_exp_f32_e32 v74, v74
	v_exp_f32_e32 v75, v75
	v_cvt_pk_f16_f32 v164, v72, v73
	v_add_f32_e32 v72, v72, v73
	v_add_f32_e32 v231, v231, v70
	v_mfma_f32_32x32x16_f16 v[32:47], v[200:203], v[172:175], v[32:47]
	ds_read_b128 v[200:203], v226 offset:27680
	v_exp_f32_e32 v76, v76
	v_exp_f32_e32 v77, v77
	v_cvt_pk_f16_f32 v165, v74, v75
	v_add_f32_e32 v74, v74, v75
	v_add_f32_e32 v231, v231, v72
	v_mfma_f32_32x32x16_f16 v[48:63], v[204:207], v[172:175], v[48:63]
	ds_read_b128 v[204:207], v226 offset:32288
	v_exp_f32_e32 v78, v78
	v_exp_f32_e32 v79, v79
	v_cvt_pk_f16_f32 v166, v76, v77
	v_add_f32_e32 v76, v76, v77
	v_add_f32_e32 v231, v231, v74
	v_cvt_pk_f16_f32 v167, v78, v79
	v_add_f32_e32 v78, v78, v79
	v_add_f32_e32 v231, v231, v76
	v_add_f32_e32 v231, v231, v78
	v_cmp_nge_f32_e32 vcc, s34, v231
	s_cbranch_vccnz .Lovf_a30

.Lovfret_b30:
	v_add_f32_e32 v233, v233, v231
	s_waitcnt lgkmcnt(0)
	v_mfma_f32_32x32x16_f16 v[80:95], v[176:179], v[144:147], v[112:127]
	ds_read_b128 v[176:179], v225 offset:0
	s_waitcnt vmcnt(3)
	v_exp_f32_e32 v64, v64
	v_exp_f32_e32 v65, v65
	v_cvt_pk_f16_f32 v216, v216, v217
	v_cvt_pk_f16_f32 v217, v218, v219
	v_mfma_f32_32x32x16_f16 v[80:95], v[180:183], v[148:151], v[80:95]
	ds_read_b128 v[180:183], v225 offset:32
	v_exp_f32_e32 v66, v66
	v_exp_f32_e32 v67, v67
	v_cvt_pk_f16_f32 v218, v220, v221
	v_cvt_pk_f16_f32 v160, v64, v65
	v_add_f32_e32 v64, v64, v65
	v_cvt_pk_f16_f32 v219, v222, v223
	v_mfma_f32_32x32x16_f16 v[80:95], v[184:187], v[152:155], v[80:95]
	ds_write_b128 v228, v[216:219] offset:0
	ds_read_b128 v[184:187], v225 offset:64
	v_exp_f32_e32 v68, v68
	v_exp_f32_e32 v69, v69
	v_cvt_pk_f16_f32 v161, v66, v67
	v_add_f32_e32 v66, v66, v67
	v_mfma_f32_32x32x16_f16 v[80:95], v[188:191], v[156:159], v[80:95]
	ds_read_b128 v[188:191], v225 offset:96
	v_exp_f32_e32 v70, v70
	v_exp_f32_e32 v71, v71
	v_cvt_pk_f16_f32 v162, v68, v69
	v_add_f32_e32 v68, v68, v69
	v_add_f32_e32 v231, v64, v66
	v_mfma_f32_32x32x16_f16 v[32:47], v[192:195], v[168:171], v[32:47]
	ds_read_b128 v[192:195], v226 offset:27712
	v_exp_f32_e32 v72, v72
	v_exp_f32_e32 v73, v73
	v_cvt_pk_f16_f32 v163, v70, v71
	v_add_f32_e32 v70, v70, v71
	v_add_f32_e32 v231, v231, v68
	v_mfma_f32_32x32x16_f16 v[48:63], v[196:199], v[168:171], v[48:63]
	ds_read_b128 v[196:199], v226 offset:32320
	v_exp_f32_e32 v74, v74
	v_exp_f32_e32 v75, v75
	v_cvt_pk_f16_f32 v164, v72, v73
	v_add_f32_e32 v72, v72, v73
	v_add_f32_e32 v231, v231, v70
	v_mfma_f32_32x32x16_f16 v[32:47], v[200:203], v[172:175], v[32:47]
	ds_read_b128 v[200:203], v226 offset:27744
	v_exp_f32_e32 v76, v76
	v_exp_f32_e32 v77, v77
	v_cvt_pk_f16_f32 v165, v74, v75
	v_add_f32_e32 v74, v74, v75
	v_add_f32_e32 v231, v231, v72
	v_mfma_f32_32x32x16_f16 v[48:63], v[204:207], v[172:175], v[48:63]
	ds_read_b128 v[204:207], v226 offset:32352
	v_exp_f32_e32 v78, v78
	v_exp_f32_e32 v79, v79
	v_cvt_pk_f16_f32 v166, v76, v77
	v_add_f32_e32 v76, v76, v77
	v_add_f32_e32 v231, v231, v74
	v_cvt_pk_f16_f32 v167, v78, v79
	v_add_f32_e32 v78, v78, v79
	v_add_f32_e32 v231, v231, v76
	v_add_f32_e32 v231, v231, v78
	v_cmp_nge_f32_e32 vcc, s34, v231
	s_cbranch_vccnz .Lovf_a31

.Lovfret_b31:
	v_add_f32_e32 v233, v233, v231
	s_waitcnt lgkmcnt(6)
	s_barrier
	s_add_u32 s23, s23, 1
	s_add_u32 s27, s27, 1
	s_cmp_eq_u32 s27, 7
	s_cbranch_scc0 .Lbody
	s_nop 15
	s_nop 7
	v_mov_b32_e32 v235, v232
	v_mov_b32_e32 v236, v232
	s_nop 1
	v_permlane32_swap_b32_e32 v235, v236
	v_add_f32_e32 v236, v235, v236
	v_rcp_f32_e32 v237, v236
	s_nop 0
	v_fma_f32 v238, -v236, v237, 1.0
	v_fmac_f32_e32 v237, v238, v237
	v_mul_f32_e32 v0, v237, v0
	v_mul_f32_e32 v1, v237, v1
	v_mul_f32_e32 v2, v237, v2
	v_mul_f32_e32 v3, v237, v3
	v_mul_f32_e32 v4, v237, v4
	v_mul_f32_e32 v5, v237, v5
	v_mul_f32_e32 v6, v237, v6
	v_mul_f32_e32 v7, v237, v7
	v_mul_f32_e32 v8, v237, v8
	v_mul_f32_e32 v9, v237, v9
	v_mul_f32_e32 v10, v237, v10
	v_mul_f32_e32 v11, v237, v11
	v_mul_f32_e32 v12, v237, v12
	v_mul_f32_e32 v13, v237, v13
	v_mul_f32_e32 v14, v237, v14
	v_mul_f32_e32 v15, v237, v15
	v_mul_f32_e32 v16, v237, v16
	v_mul_f32_e32 v17, v237, v17
	v_mul_f32_e32 v18, v237, v18
	v_mul_f32_e32 v19, v237, v19
	v_mul_f32_e32 v20, v237, v20
	v_mul_f32_e32 v21, v237, v21
	v_mul_f32_e32 v22, v237, v22
	v_mul_f32_e32 v23, v237, v23
	v_mul_f32_e32 v24, v237, v24
	v_mul_f32_e32 v25, v237, v25
	v_mul_f32_e32 v26, v237, v26
	v_mul_f32_e32 v27, v237, v27
	v_mul_f32_e32 v28, v237, v28
	v_mul_f32_e32 v29, v237, v29
	v_mul_f32_e32 v30, v237, v30
	v_mul_f32_e32 v31, v237, v31
	ds_write_b128 v241, v[0:3] offset:0
	ds_write_b128 v241, v[16:19] offset:128
	ds_write_b128 v241, v[4:7] offset:32
	ds_write_b128 v241, v[20:23] offset:160
	ds_write_b128 v241, v[8:11] offset:64
	ds_write_b128 v241, v[24:27] offset:192
	ds_write_b128 v241, v[12:15] offset:96
	ds_write_b128 v241, v[28:31] offset:224
	s_waitcnt lgkmcnt(0)
	ds_read_b128 v[0:3], v242 offset:0
	ds_read_b128 v[4:7], v242 offset:1088
	ds_read_b128 v[8:11], v242 offset:2176
	ds_read_b128 v[12:15], v242 offset:3264
	ds_read_b128 v[16:19], v242 offset:4352
	ds_read_b128 v[20:23], v242 offset:5440
	ds_read_b128 v[24:27], v242 offset:6528
	ds_read_b128 v[28:31], v242 offset:7616
	s_waitcnt lgkmcnt(7)
	s_add_u32 s31, s30, 0x0
	buffer_store_dwordx4 v[0:3], v244, s[12:15], s31 offen nt sc1
	s_waitcnt lgkmcnt(6)
	s_add_u32 s31, s30, 0x4000
	buffer_store_dwordx4 v[4:7], v244, s[12:15], s31 offen nt sc1
	s_waitcnt lgkmcnt(5)
	s_add_u32 s31, s30, 0x8000
	buffer_store_dwordx4 v[8:11], v244, s[12:15], s31 offen nt sc1
	s_waitcnt lgkmcnt(4)
	s_add_u32 s31, s30, 0xc000
	buffer_store_dwordx4 v[12:15], v244, s[12:15], s31 offen nt sc1
	s_waitcnt lgkmcnt(3)
	s_add_u32 s31, s30, 0x10000
	buffer_store_dwordx4 v[16:19], v244, s[12:15], s31 offen nt sc1
	s_waitcnt lgkmcnt(2)
	s_add_u32 s31, s30, 0x14000
	buffer_store_dwordx4 v[20:23], v244, s[12:15], s31 offen nt sc1
	s_waitcnt lgkmcnt(1)
	s_add_u32 s31, s30, 0x18000
	buffer_store_dwordx4 v[24:27], v244, s[12:15], s31 offen nt sc1
	s_waitcnt lgkmcnt(0)
	s_add_u32 s31, s30, 0x1c000
	buffer_store_dwordx4 v[28:31], v244, s[12:15], s31 offen nt sc1
	s_nop 1
	s_waitcnt lgkmcnt(0)
	v_mfma_f32_32x32x16_f16 v[80:95], v[176:179], v[144:147], v[112:127]
	ds_read_b128 v[176:179], v225 offset:4608
	v_mfma_f32_32x32x16_f16 v[80:95], v[180:183], v[148:151], v[80:95]
	ds_read_b128 v[180:183], v225 offset:4640
	v_mfma_f32_32x32x16_f16 v[80:95], v[184:187], v[152:155], v[80:95]
	ds_read_b128 v[184:187], v225 offset:4672
	v_mfma_f32_32x32x16_f16 v[80:95], v[188:191], v[156:159], v[80:95]
	ds_read_b128 v[188:191], v225 offset:4704
	s_nop 15
	s_nop 3
	s_waitcnt vmcnt(8)
	v_cmp_ne_u32_e64 s[20:21], 0, v224
	s_add_u32 s31, s23, 1
	s_and_b32 s31, s31, 31
	s_lshl_b32 s31, s31, 8
	s_add_u32 s26, s31, s22
	s_add_u32 s31, s23, 3
	s_and_b32 s31, s31, 31
	s_mul_i32 s31, s31, 0xc0000
	s_add_u32 s24, s31, s18
	s_add_u32 s31, s23, 2
	s_and_b32 s31, s31, 31
	s_mul_i32 s31, s31, 0xc0000
	s_add_u32 s25, s31, s19
	s_cmp_eq_u64 s[20:21], -1
	s_cselect_b32 s34, s37, s38
	s_waitcnt lgkmcnt(0)
	v_mfma_f32_32x32x16_f16 v[64:79], v[176:179], v[144:147], v[112:127]
	ds_read_b128 v[176:179], v225 offset:9216
	buffer_load_dword v224, v230, s[8:11], s26 offen
	v_exp_f32_e32 v80, v80
	v_exp_f32_e32 v81, v81
	v_cvt_pk_f16_f32 v208, v208, v209
	v_cvt_pk_f16_f32 v209, v210, v211
	v_mfma_f32_32x32x16_f16 v[64:79], v[180:183], v[148:151], v[64:79]
	ds_read_b128 v[180:183], v225 offset:9248
	v_exp_f32_e32 v82, v82
	v_exp_f32_e32 v83, v83
	v_cvt_pk_f16_f32 v212, v212, v213
	v_cvt_pk_f16_f32 v160, v80, v81
	v_add_f32_e32 v80, v80, v81
	v_cvt_pk_f16_f32 v213, v214, v215
	v_mfma_f32_32x32x16_f16 v[64:79], v[184:187], v[152:155], v[64:79]
	ds_write_b64 v227, v[208:209] offset:18432
	ds_write_b64 v227, v[212:213] offset:23040
	ds_read_b128 v[184:187], v225 offset:9280
	v_exp_f32_e32 v84, v84
	v_exp_f32_e32 v85, v85
	v_cvt_pk_f16_f32 v161, v82, v83
	v_add_f32_e32 v82, v82, v83
	v_mfma_f32_32x32x16_f16 v[64:79], v[188:191], v[156:159], v[64:79]
	ds_read_b128 v[188:191], v225 offset:9312
	buffer_load_dwordx4 v[208:211], v229, s[4:7], s24 offen
	v_exp_f32_e32 v86, v86
	v_exp_f32_e32 v87, v87
	v_cvt_pk_f16_f32 v162, v84, v85
	v_add_f32_e32 v84, v84, v85
	v_add_f32_e32 v231, v80, v82
	s_waitcnt lgkmcnt(10)
	v_mfma_f32_32x32x16_f16 v[32:47], v[192:195], v[168:171], v[32:47]
	ds_read_b128 v[192:195], v226 offset:0
	buffer_load_dwordx4 v[212:215], v252, s[4:7], s24 offen
	v_exp_f32_e32 v88, v88
	v_exp_f32_e32 v89, v89
	v_cvt_pk_f16_f32 v163, v86, v87
	v_add_f32_e32 v86, v86, v87
	v_add_f32_e32 v231, v231, v84
	v_mfma_f32_32x32x16_f16 v[48:63], v[196:199], v[168:171], v[48:63]
	ds_read_b128 v[196:199], v226 offset:4608
	v_exp_f32_e32 v90, v90
	v_exp_f32_e32 v91, v91
	v_cvt_pk_f16_f32 v164, v88, v89
	v_add_f32_e32 v88, v88, v89
	v_add_f32_e32 v231, v231, v86
	v_mfma_f32_32x32x16_f16 v[32:47], v[200:203], v[172:175], v[32:47]
	ds_read_b128 v[200:203], v226 offset:32
	v_exp_f32_e32 v92, v92
	v_exp_f32_e32 v93, v93
	v_cvt_pk_f16_f32 v165, v90, v91
	v_add_f32_e32 v90, v90, v91
	v_add_f32_e32 v231, v231, v88
	v_mfma_f32_32x32x16_f16 v[48:63], v[204:207], v[172:175], v[48:63]
	ds_read_b128 v[204:207], v226 offset:4640
	v_exp_f32_e32 v94, v94
	v_exp_f32_e32 v95, v95
	v_cvt_pk_f16_f32 v166, v92, v93
	v_add_f32_e32 v92, v92, v93
	v_add_f32_e32 v231, v231, v90
	v_cvt_pk_f16_f32 v167, v94, v95
	v_add_f32_e32 v94, v94, v95
	v_add_f32_e32 v231, v231, v92
	v_add_f32_e32 v231, v231, v94
	v_cmp_nge_f32_e32 vcc, s34, v231
	s_cbranch_vccnz .Lovf_b1_00
.Lovfret_b1_00:
	v_add_f32_e32 v233, v233, v231
	s_waitcnt lgkmcnt(4)
	v_mfma_f32_32x32x16_f16 v[80:95], v[176:179], v[144:147], v[112:127]
	ds_read_b128 v[176:179], v225 offset:13824
	s_waitcnt vmcnt(3)
	v_exp_f32_e32 v64, v64
	v_exp_f32_e32 v65, v65
	v_cvt_pk_f16_f32 v216, v216, v217
	v_cvt_pk_f16_f32 v217, v218, v219
	v_mfma_f32_32x32x16_f16 v[80:95], v[180:183], v[148:151], v[80:95]
	ds_read_b128 v[180:183], v225 offset:13856
	v_exp_f32_e32 v66, v66
	v_exp_f32_e32 v67, v67
	v_cvt_pk_f16_f32 v218, v220, v221
	v_cvt_pk_f16_f32 v168, v64, v65
	v_add_f32_e32 v64, v64, v65
	v_cvt_pk_f16_f32 v219, v222, v223
	v_mfma_f32_32x32x16_f16 v[80:95], v[184:187], v[152:155], v[80:95]
	ds_write_b128 v228, v[216:219] offset:9216
	ds_read_b128 v[184:187], v225 offset:13888
	v_exp_f32_e32 v68, v68
	v_exp_f32_e32 v69, v69
	v_cvt_pk_f16_f32 v169, v66, v67
	v_add_f32_e32 v66, v66, v67
	v_mfma_f32_32x32x16_f16 v[80:95], v[188:191], v[156:159], v[80:95]
	ds_read_b128 v[188:191], v225 offset:13920
	buffer_load_dword v216, v230, s[4:7], s25 offen
	buffer_load_dword v217, v245, s[4:7], s25 offen
	v_exp_f32_e32 v70, v70
	v_exp_f32_e32 v71, v71
	v_cvt_pk_f16_f32 v170, v68, v69
	v_add_f32_e32 v68, v68, v69
	v_add_f32_e32 v231, v64, v66
	s_waitcnt lgkmcnt(5)
	v_mfma_f32_32x32x16_f16 v[32:47], v[192:195], v[160:163], v[32:47]
	ds_read_b128 v[192:195], v226 offset:64
	buffer_load_dword v218, v246, s[4:7], s25 offen
	buffer_load_dword v219, v247, s[4:7], s25 offen
	v_exp_f32_e32 v72, v72
	v_exp_f32_e32 v73, v73
	v_cvt_pk_f16_f32 v171, v70, v71
	v_add_f32_e32 v70, v70, v71
	v_add_f32_e32 v231, v231, v68
	v_mfma_f32_32x32x16_f16 v[48:63], v[196:199], v[160:163], v[48:63]
	ds_read_b128 v[196:199], v226 offset:4672
	buffer_load_dword v220, v248, s[4:7], s25 offen
	buffer_load_dword v221, v249, s[4:7], s25 offen
	v_exp_f32_e32 v74, v74
	v_exp_f32_e32 v75, v75
	v_cvt_pk_f16_f32 v172, v72, v73
	v_add_f32_e32 v72, v72, v73
	v_add_f32_e32 v231, v231, v70
	v_mfma_f32_32x32x16_f16 v[32:47], v[200:203], v[164:167], v[32:47]
	ds_read_b128 v[200:203], v226 offset:96
	buffer_load_dword v222, v250, s[4:7], s25 offen
	v_exp_f32_e32 v76, v76
	v_exp_f32_e32 v77, v77
	v_cvt_pk_f16_f32 v173, v74, v75
	v_add_f32_e32 v74, v74, v75
	v_add_f32_e32 v231, v231, v72
	v_mfma_f32_32x32x16_f16 v[48:63], v[204:207], v[164:167], v[48:63]
	ds_read_b128 v[204:207], v226 offset:4704
	buffer_load_dword v223, v251, s[4:7], s25 offen
	v_exp_f32_e32 v78, v78
	v_exp_f32_e32 v79, v79
	v_cvt_pk_f16_f32 v174, v76, v77
	v_add_f32_e32 v76, v76, v77
	v_add_f32_e32 v231, v231, v74
	v_cvt_pk_f16_f32 v175, v78, v79
	v_add_f32_e32 v78, v78, v79
	v_add_f32_e32 v231, v231, v76
	v_add_f32_e32 v231, v231, v78
	v_cmp_nge_f32_e32 vcc, s34, v231
	s_cbranch_vccnz .Lovf_b1_01
.Lovfret_b1_01:
	v_add_f32_e32 v233, v233, v231
	s_waitcnt lgkmcnt(6)
	s_barrier
	s_add_u32 s23, s23, 1
	s_waitcnt vmcnt(8)
	v_cmp_ne_u32_e64 s[20:21], 0, v224
	s_add_u32 s31, s23, 1
	s_and_b32 s31, s31, 31
	s_lshl_b32 s31, s31, 8
	s_add_u32 s26, s31, s22
	s_add_u32 s31, s23, 3
	s_and_b32 s31, s31, 31
	s_mul_i32 s31, s31, 0xc0000
	s_add_u32 s24, s31, s18
	s_add_u32 s31, s23, 2
	s_and_b32 s31, s31, 31
	s_mul_i32 s31, s31, 0xc0000
	s_add_u32 s25, s31, s19
	s_cmp_eq_u64 s[20:21], -1
	s_cselect_b32 s34, s37, s38
	s_waitcnt lgkmcnt(4)
	v_mfma_f32_32x32x16_f16 v[64:79], v[176:179], v[144:147], v[112:127]
	ds_read_b128 v[176:179], v225 offset:18432
	buffer_load_dword v224, v230, s[8:11], s26 offen
	v_exp_f32_e32 v80, v80
	v_exp_f32_e32 v81, v81
	v_cvt_pk_f16_f32 v208, v208, v209
	v_cvt_pk_f16_f32 v209, v210, v211
	v_mfma_f32_32x32x16_f16 v[64:79], v[180:183], v[148:151], v[64:79]
	ds_read_b128 v[180:183], v225 offset:18464
	v_exp_f32_e32 v82, v82
	v_exp_f32_e32 v83, v83
	v_cvt_pk_f16_f32 v212, v212, v213
	v_cvt_pk_f16_f32 v160, v80, v81
	v_add_f32_e32 v80, v80, v81
	v_cvt_pk_f16_f32 v213, v214, v215
	v_mfma_f32_32x32x16_f16 v[64:79], v[184:187], v[152:155], v[64:79]
	ds_write_b64 v227, v[208:209] offset:27648
	ds_write_b64 v227, v[212:213] offset:32256
	ds_read_b128 v[184:187], v225 offset:18496
	v_exp_f32_e32 v84, v84
	v_exp_f32_e32 v85, v85
	v_cvt_pk_f16_f32 v161, v82, v83
	v_add_f32_e32 v82, v82, v83
	v_mfma_f32_32x32x16_f16 v[64:79], v[188:191], v[156:159], v[64:79]
	ds_read_b128 v[188:191], v225 offset:18528
	buffer_load_dwordx4 v[208:211], v229, s[4:7], s24 offen
	v_exp_f32_e32 v86, v86
	v_exp_f32_e32 v87, v87
	v_cvt_pk_f16_f32 v162, v84, v85
	v_add_f32_e32 v84, v84, v85
	v_add_f32_e32 v231, v80, v82
	s_waitcnt lgkmcnt(6)
	v_mfma_f32_32x32x16_f16 v[32:47], v[192:195], v[168:171], v[32:47]
	ds_read_b128 v[192:195], v226 offset:9216
	buffer_load_dwordx4 v[212:215], v252, s[4:7], s24 offen
	v_exp_f32_e32 v88, v88
	v_exp_f32_e32 v89, v89
	v_cvt_pk_f16_f32 v163, v86, v87
	v_add_f32_e32 v86, v86, v87
	v_add_f32_e32 v231, v231, v84
	v_mfma_f32_32x32x16_f16 v[48:63], v[196:199], v[168:171], v[48:63]
	ds_read_b128 v[196:199], v226 offset:13824
	v_exp_f32_e32 v90, v90
	v_exp_f32_e32 v91, v91
	v_cvt_pk_f16_f32 v164, v88, v89
	v_add_f32_e32 v88, v88, v89
	v_add_f32_e32 v231, v231, v86
	v_mfma_f32_32x32x16_f16 v[32:47], v[200:203], v[172:175], v[32:47]
	ds_read_b128 v[200:203], v226 offset:9248
	v_exp_f32_e32 v92, v92
	v_exp_f32_e32 v93, v93
	v_cvt_pk_f16_f32 v165, v90, v91
	v_add_f32_e32 v90, v90, v91
	v_add_f32_e32 v231, v231, v88
	v_mfma_f32_32x32x16_f16 v[48:63], v[204:207], v[172:175], v[48:63]
	ds_read_b128 v[204:207], v226 offset:13856
	v_exp_f32_e32 v94, v94
	v_exp_f32_e32 v95, v95
	v_cvt_pk_f16_f32 v166, v92, v93
	v_add_f32_e32 v92, v92, v93
	v_add_f32_e32 v231, v231, v90
	v_cvt_pk_f16_f32 v167, v94, v95
	v_add_f32_e32 v94, v94, v95
	v_add_f32_e32 v231, v231, v92
	v_add_f32_e32 v231, v231, v94
	v_cmp_nge_f32_e32 vcc, s34, v231
	s_cbranch_vccnz .Lovf_b1_10
.Lovfret_b1_10:
	v_add_f32_e32 v233, v233, v231
	s_waitcnt lgkmcnt(4)
	v_mfma_f32_32x32x16_f16 v[80:95], v[176:179], v[144:147], v[112:127]
	ds_read_b128 v[176:179], v225 offset:23040
	s_waitcnt vmcnt(3)
	v_exp_f32_e32 v64, v64
	v_exp_f32_e32 v65, v65
	v_cvt_pk_f16_f32 v216, v216, v217
	v_cvt_pk_f16_f32 v217, v218, v219
	v_mfma_f32_32x32x16_f16 v[80:95], v[180:183], v[148:151], v[80:95]
	ds_read_b128 v[180:183], v225 offset:23072
	v_exp_f32_e32 v66, v66
	v_exp_f32_e32 v67, v67
	v_cvt_pk_f16_f32 v218, v220, v221
	v_cvt_pk_f16_f32 v168, v64, v65
	v_add_f32_e32 v64, v64, v65
	v_cvt_pk_f16_f32 v219, v222, v223
	v_mfma_f32_32x32x16_f16 v[80:95], v[184:187], v[152:155], v[80:95]
	ds_write_b128 v228, v[216:219] offset:18432
	ds_read_b128 v[184:187], v225 offset:23104
	v_exp_f32_e32 v68, v68
	v_exp_f32_e32 v69, v69
	v_cvt_pk_f16_f32 v169, v66, v67
	v_add_f32_e32 v66, v66, v67
	v_mfma_f32_32x32x16_f16 v[80:95], v[188:191], v[156:159], v[80:95]
	ds_read_b128 v[188:191], v225 offset:23136
	buffer_load_dword v216, v230, s[4:7], s25 offen
	buffer_load_dword v217, v245, s[4:7], s25 offen
	v_exp_f32_e32 v70, v70
	v_exp_f32_e32 v71, v71
	v_cvt_pk_f16_f32 v170, v68, v69
	v_add_f32_e32 v68, v68, v69
	v_add_f32_e32 v231, v64, v66
	s_waitcnt lgkmcnt(5)
	v_mfma_f32_32x32x16_f16 v[32:47], v[192:195], v[160:163], v[32:47]
	ds_read_b128 v[192:195], v226 offset:9280
	buffer_load_dword v218, v246, s[4:7], s25 offen
	buffer_load_dword v219, v247, s[4:7], s25 offen
	v_exp_f32_e32 v72, v72
	v_exp_f32_e32 v73, v73
	v_cvt_pk_f16_f32 v171, v70, v71
	v_add_f32_e32 v70, v70, v71
	v_add_f32_e32 v231, v231, v68
	v_mfma_f32_32x32x16_f16 v[48:63], v[196:199], v[160:163], v[48:63]
	ds_read_b128 v[196:199], v226 offset:13888
	buffer_load_dword v220, v248, s[4:7], s25 offen
	buffer_load_dword v221, v249, s[4:7], s25 offen
	v_exp_f32_e32 v74, v74
	v_exp_f32_e32 v75, v75
	v_cvt_pk_f16_f32 v172, v72, v73
	v_add_f32_e32 v72, v72, v73
	v_add_f32_e32 v231, v231, v70
	v_mfma_f32_32x32x16_f16 v[32:47], v[200:203], v[164:167], v[32:47]
	ds_read_b128 v[200:203], v226 offset:9312
	buffer_load_dword v222, v250, s[4:7], s25 offen
	v_exp_f32_e32 v76, v76
	v_exp_f32_e32 v77, v77
	v_cvt_pk_f16_f32 v173, v74, v75
	v_add_f32_e32 v74, v74, v75
	v_add_f32_e32 v231, v231, v72
	v_mfma_f32_32x32x16_f16 v[48:63], v[204:207], v[164:167], v[48:63]
	ds_read_b128 v[204:207], v226 offset:13920
	buffer_load_dword v223, v251, s[4:7], s25 offen
	v_exp_f32_e32 v78, v78
	v_exp_f32_e32 v79, v79
	v_cvt_pk_f16_f32 v174, v76, v77
	v_add_f32_e32 v76, v76, v77
	v_add_f32_e32 v231, v231, v74
	v_cvt_pk_f16_f32 v175, v78, v79
	v_add_f32_e32 v78, v78, v79
	v_add_f32_e32 v231, v231, v76
	v_add_f32_e32 v231, v231, v78
	v_cmp_nge_f32_e32 vcc, s34, v231
	s_cbranch_vccnz .Lovf_b1_11
.Lovfret_b1_11:
	v_add_f32_e32 v233, v233, v231
	s_waitcnt lgkmcnt(6)
	s_barrier
	s_add_u32 s23, s23, 1
	s_waitcnt vmcnt(8)
	v_cmp_ne_u32_e64 s[20:21], 0, v224
	s_add_u32 s31, s23, 1
	s_and_b32 s31, s31, 31
	s_lshl_b32 s31, s31, 8
	s_add_u32 s26, s31, s22
	s_add_u32 s31, s23, 3
	s_and_b32 s31, s31, 31
	s_mul_i32 s31, s31, 0xc0000
	s_add_u32 s24, s31, s18
	s_add_u32 s31, s23, 2
	s_and_b32 s31, s31, 31
	s_mul_i32 s31, s31, 0xc0000
	s_add_u32 s25, s31, s19
	s_cmp_eq_u64 s[20:21], -1
	s_cselect_b32 s34, s37, s38
	s_waitcnt lgkmcnt(4)
	v_mfma_f32_32x32x16_f16 v[64:79], v[176:179], v[144:147], v[112:127]
	ds_read_b128 v[176:179], v225 offset:27648
	buffer_load_dword v224, v230, s[8:11], s26 offen
	v_exp_f32_e32 v80, v80
	v_exp_f32_e32 v81, v81
	v_cvt_pk_f16_f32 v208, v208, v209
	v_cvt_pk_f16_f32 v209, v210, v211
	v_mfma_f32_32x32x16_f16 v[64:79], v[180:183], v[148:151], v[64:79]
	ds_read_b128 v[180:183], v225 offset:27680
	v_exp_f32_e32 v82, v82
	v_exp_f32_e32 v83, v83
	v_cvt_pk_f16_f32 v212, v212, v213
	v_cvt_pk_f16_f32 v160, v80, v81
	v_add_f32_e32 v80, v80, v81
	v_cvt_pk_f16_f32 v213, v214, v215
	v_mfma_f32_32x32x16_f16 v[64:79], v[184:187], v[152:155], v[64:79]
	ds_write_b64 v227, v[208:209] offset:0
	ds_write_b64 v227, v[212:213] offset:4608
	ds_read_b128 v[184:187], v225 offset:27712
	v_exp_f32_e32 v84, v84
	v_exp_f32_e32 v85, v85
	v_cvt_pk_f16_f32 v161, v82, v83
	v_add_f32_e32 v82, v82, v83
	v_mfma_f32_32x32x16_f16 v[64:79], v[188:191], v[156:159], v[64:79]
	ds_read_b128 v[188:191], v225 offset:27744
	buffer_load_dwordx4 v[208:211], v229, s[4:7], s24 offen
	v_exp_f32_e32 v86, v86
	v_exp_f32_e32 v87, v87
	v_cvt_pk_f16_f32 v162, v84, v85
	v_add_f32_e32 v84, v84, v85
	v_add_f32_e32 v231, v80, v82
	s_waitcnt lgkmcnt(6)
	v_mfma_f32_32x32x16_f16 v[32:47], v[192:195], v[168:171], v[32:47]
	ds_read_b128 v[192:195], v226 offset:18432
	buffer_load_dwordx4 v[212:215], v252, s[4:7], s24 offen
	v_exp_f32_e32 v88, v88
	v_exp_f32_e32 v89, v89
	v_cvt_pk_f16_f32 v163, v86, v87
	v_add_f32_e32 v86, v86, v87
	v_add_f32_e32 v231, v231, v84
	v_mfma_f32_32x32x16_f16 v[48:63], v[196:199], v[168:171], v[48:63]
	ds_read_b128 v[196:199], v226 offset:23040
	v_exp_f32_e32 v90, v90
	v_exp_f32_e32 v91, v91
	v_cvt_pk_f16_f32 v164, v88, v89
	v_add_f32_e32 v88, v88, v89
	v_add_f32_e32 v231, v231, v86
	v_mfma_f32_32x32x16_f16 v[32:47], v[200:203], v[172:175], v[32:47]
	ds_read_b128 v[200:203], v226 offset:18464
	v_exp_f32_e32 v92, v92
	v_exp_f32_e32 v93, v93
	v_cvt_pk_f16_f32 v165, v90, v91
	v_add_f32_e32 v90, v90, v91
	v_add_f32_e32 v231, v231, v88
	v_mfma_f32_32x32x16_f16 v[48:63], v[204:207], v[172:175], v[48:63]
	ds_read_b128 v[204:207], v226 offset:23072
	v_exp_f32_e32 v94, v94
	v_exp_f32_e32 v95, v95
	v_cvt_pk_f16_f32 v166, v92, v93
	v_add_f32_e32 v92, v92, v93
	v_add_f32_e32 v231, v231, v90
	v_cvt_pk_f16_f32 v167, v94, v95
	v_add_f32_e32 v94, v94, v95
	v_add_f32_e32 v231, v231, v92
	v_add_f32_e32 v231, v231, v94
	v_cmp_nge_f32_e32 vcc, s34, v231
	s_cbranch_vccnz .Lovf_b1_20
.Lovfret_b1_20:
	v_add_f32_e32 v233, v233, v231
	s_waitcnt lgkmcnt(4)
	v_mfma_f32_32x32x16_f16 v[80:95], v[176:179], v[144:147], v[112:127]
	ds_read_b128 v[176:179], v225 offset:32256
	s_waitcnt vmcnt(3)
	v_exp_f32_e32 v64, v64
	v_exp_f32_e32 v65, v65
	v_cvt_pk_f16_f32 v216, v216, v217
	v_cvt_pk_f16_f32 v217, v218, v219
	v_mfma_f32_32x32x16_f16 v[80:95], v[180:183], v[148:151], v[80:95]
	ds_read_b128 v[180:183], v225 offset:32288
	v_exp_f32_e32 v66, v66
	v_exp_f32_e32 v67, v67
	v_cvt_pk_f16_f32 v218, v220, v221
	v_cvt_pk_f16_f32 v168, v64, v65
	v_add_f32_e32 v64, v64, v65
	v_cvt_pk_f16_f32 v219, v222, v223
	v_mfma_f32_32x32x16_f16 v[80:95], v[184:187], v[152:155], v[80:95]
	ds_write_b128 v228, v[216:219] offset:27648
	ds_read_b128 v[184:187], v225 offset:32320
	v_exp_f32_e32 v68, v68
	v_exp_f32_e32 v69, v69
	v_cvt_pk_f16_f32 v169, v66, v67
	v_add_f32_e32 v66, v66, v67
	v_mfma_f32_32x32x16_f16 v[80:95], v[188:191], v[156:159], v[80:95]
	ds_read_b128 v[188:191], v225 offset:32352
	buffer_load_dword v216, v230, s[4:7], s25 offen
	buffer_load_dword v217, v245, s[4:7], s25 offen
	v_exp_f32_e32 v70, v70
	v_exp_f32_e32 v71, v71
	v_cvt_pk_f16_f32 v170, v68, v69
	v_add_f32_e32 v68, v68, v69
	v_add_f32_e32 v231, v64, v66
	s_waitcnt lgkmcnt(5)
	v_mfma_f32_32x32x16_f16 v[32:47], v[192:195], v[160:163], v[32:47]
	ds_read_b128 v[192:195], v226 offset:18496
	buffer_load_dword v218, v246, s[4:7], s25 offen
	buffer_load_dword v219, v247, s[4:7], s25 offen
	v_exp_f32_e32 v72, v72
	v_exp_f32_e32 v73, v73
	v_cvt_pk_f16_f32 v171, v70, v71
	v_add_f32_e32 v70, v70, v71
	v_add_f32_e32 v231, v231, v68
	v_mfma_f32_32x32x16_f16 v[48:63], v[196:199], v[160:163], v[48:63]
	ds_read_b128 v[196:199], v226 offset:23104
	buffer_load_dword v220, v248, s[4:7], s25 offen
	buffer_load_dword v221, v249, s[4:7], s25 offen
	v_exp_f32_e32 v74, v74
	v_exp_f32_e32 v75, v75
	v_cvt_pk_f16_f32 v172, v72, v73
	v_add_f32_e32 v72, v72, v73
	v_add_f32_e32 v231, v231, v70
	v_mfma_f32_32x32x16_f16 v[32:47], v[200:203], v[164:167], v[32:47]
	ds_read_b128 v[200:203], v226 offset:18528
	buffer_load_dword v222, v250, s[4:7], s25 offen
	v_exp_f32_e32 v76, v76
	v_exp_f32_e32 v77, v77
	v_cvt_pk_f16_f32 v173, v74, v75
	v_add_f32_e32 v74, v74, v75
	v_add_f32_e32 v231, v231, v72
	v_mfma_f32_32x32x16_f16 v[48:63], v[204:207], v[164:167], v[48:63]
	ds_read_b128 v[204:207], v226 offset:23136
	buffer_load_dword v223, v251, s[4:7], s25 offen
	v_exp_f32_e32 v78, v78
	v_exp_f32_e32 v79, v79
	v_cvt_pk_f16_f32 v174, v76, v77
	v_add_f32_e32 v76, v76, v77
	v_add_f32_e32 v231, v231, v74
	v_cvt_pk_f16_f32 v175, v78, v79
	v_add_f32_e32 v78, v78, v79
	v_add_f32_e32 v231, v231, v76
	v_add_f32_e32 v231, v231, v78
	v_cmp_nge_f32_e32 vcc, s34, v231
	s_cbranch_vccnz .Lovf_b1_21
.Lovfret_b1_21:
	v_add_f32_e32 v233, v233, v231
	s_waitcnt lgkmcnt(6)
	s_barrier
	s_add_u32 s23, s23, 1
	s_waitcnt vmcnt(8)
	v_cmp_ne_u32_e64 s[20:21], 0, v224
	s_add_u32 s31, s23, 1
	s_and_b32 s31, s31, 31
	s_lshl_b32 s31, s31, 8
	s_add_u32 s26, s31, s22
	s_add_u32 s31, s23, 3
	s_and_b32 s31, s31, 31
	s_mul_i32 s31, s31, 0xc0000
	s_add_u32 s24, s31, s18
	s_add_u32 s31, s23, 2
	s_and_b32 s31, s31, 31
	s_mul_i32 s31, s31, 0xc0000
	s_add_u32 s25, s31, s19
	s_cmp_eq_u64 s[20:21], -1
	s_cselect_b32 s34, s37, s38
	s_waitcnt lgkmcnt(4)
	v_mfma_f32_32x32x16_f16 v[64:79], v[176:179], v[144:147], v[112:127]
	ds_read_b128 v[176:179], v225 offset:0
	buffer_load_dword v224, v230, s[8:11], s26 offen
	v_exp_f32_e32 v80, v80
	v_exp_f32_e32 v81, v81
	v_cvt_pk_f16_f32 v208, v208, v209
	v_cvt_pk_f16_f32 v209, v210, v211
	v_mfma_f32_32x32x16_f16 v[64:79], v[180:183], v[148:151], v[64:79]
	ds_read_b128 v[180:183], v225 offset:32
	v_exp_f32_e32 v82, v82
	v_exp_f32_e32 v83, v83
	v_cvt_pk_f16_f32 v212, v212, v213
	v_cvt_pk_f16_f32 v160, v80, v81
	v_add_f32_e32 v80, v80, v81
	v_cvt_pk_f16_f32 v213, v214, v215
	v_mfma_f32_32x32x16_f16 v[64:79], v[184:187], v[152:155], v[64:79]
	ds_write_b64 v227, v[208:209] offset:9216
	ds_write_b64 v227, v[212:213] offset:13824
	ds_read_b128 v[184:187], v225 offset:64
	v_exp_f32_e32 v84, v84
	v_exp_f32_e32 v85, v85
	v_cvt_pk_f16_f32 v161, v82, v83
	v_add_f32_e32 v82, v82, v83
	v_mfma_f32_32x32x16_f16 v[64:79], v[188:191], v[156:159], v[64:79]
	ds_read_b128 v[188:191], v225 offset:96
	buffer_load_dwordx4 v[208:211], v229, s[4:7], s24 offen
	v_exp_f32_e32 v86, v86
	v_exp_f32_e32 v87, v87
	v_cvt_pk_f16_f32 v162, v84, v85
	v_add_f32_e32 v84, v84, v85
	v_add_f32_e32 v231, v80, v82
	s_waitcnt lgkmcnt(6)
	v_mfma_f32_32x32x16_f16 v[32:47], v[192:195], v[168:171], v[32:47]
	ds_read_b128 v[192:195], v226 offset:27648
	buffer_load_dwordx4 v[212:215], v252, s[4:7], s24 offen
	v_exp_f32_e32 v88, v88
	v_exp_f32_e32 v89, v89
	v_cvt_pk_f16_f32 v163, v86, v87
	v_add_f32_e32 v86, v86, v87
	v_add_f32_e32 v231, v231, v84
	v_mfma_f32_32x32x16_f16 v[48:63], v[196:199], v[168:171], v[48:63]
	ds_read_b128 v[196:199], v226 offset:32256
	v_exp_f32_e32 v90, v90
	v_exp_f32_e32 v91, v91
	v_cvt_pk_f16_f32 v164, v88, v89
	v_add_f32_e32 v88, v88, v89
	v_add_f32_e32 v231, v231, v86
	v_mfma_f32_32x32x16_f16 v[32:47], v[200:203], v[172:175], v[32:47]
	ds_read_b128 v[200:203], v226 offset:27680
	v_exp_f32_e32 v92, v92
	v_exp_f32_e32 v93, v93
	v_cvt_pk_f16_f32 v165, v90, v91
	v_add_f32_e32 v90, v90, v91
	v_add_f32_e32 v231, v231, v88
	v_mfma_f32_32x32x16_f16 v[48:63], v[204:207], v[172:175], v[48:63]
	ds_read_b128 v[204:207], v226 offset:32288
	v_exp_f32_e32 v94, v94
	v_exp_f32_e32 v95, v95
	v_cvt_pk_f16_f32 v166, v92, v93
	v_add_f32_e32 v92, v92, v93
	v_add_f32_e32 v231, v231, v90
	v_cvt_pk_f16_f32 v167, v94, v95
	v_add_f32_e32 v94, v94, v95
	v_add_f32_e32 v231, v231, v92
	v_add_f32_e32 v231, v231, v94
	v_cmp_nge_f32_e32 vcc, s34, v231
	s_cbranch_vccnz .Lovf_b1_30
.Lovfret_b1_30:
	v_add_f32_e32 v233, v233, v231
	s_waitcnt vmcnt(3)
	v_exp_f32_e32 v64, v64
	v_exp_f32_e32 v65, v65
	v_cvt_pk_f16_f32 v216, v216, v217
	v_cvt_pk_f16_f32 v217, v218, v219
	v_exp_f32_e32 v66, v66
	v_exp_f32_e32 v67, v67
	v_cvt_pk_f16_f32 v218, v220, v221
	v_cvt_pk_f16_f32 v168, v64, v65
	v_add_f32_e32 v64, v64, v65
	v_cvt_pk_f16_f32 v219, v222, v223
	ds_write_b128 v228, v[216:219] offset:0
	v_exp_f32_e32 v68, v68
	v_exp_f32_e32 v69, v69
	v_cvt_pk_f16_f32 v169, v66, v67
	v_add_f32_e32 v66, v66, v67
	buffer_load_dword v216, v230, s[4:7], s25 offen
	buffer_load_dword v217, v245, s[4:7], s25 offen
	v_exp_f32_e32 v70, v70
	v_exp_f32_e32 v71, v71
	v_cvt_pk_f16_f32 v170, v68, v69
	v_add_f32_e32 v68, v68, v69
	v_add_f32_e32 v231, v64, v66
	s_waitcnt lgkmcnt(1)
	v_mfma_f32_32x32x16_f16 v[32:47], v[192:195], v[160:163], v[32:47]
	ds_read_b128 v[192:195], v226 offset:27712
	buffer_load_dword v218, v246, s[4:7], s25 offen
	buffer_load_dword v219, v247, s[4:7], s25 offen
	v_exp_f32_e32 v72, v72
	v_exp_f32_e32 v73, v73
	v_cvt_pk_f16_f32 v171, v70, v71
	v_add_f32_e32 v70, v70, v71
	v_add_f32_e32 v231, v231, v68
	v_mfma_f32_32x32x16_f16 v[48:63], v[196:199], v[160:163], v[48:63]
	ds_read_b128 v[196:199], v226 offset:32320
	buffer_load_dword v220, v248, s[4:7], s25 offen
	buffer_load_dword v221, v249, s[4:7], s25 offen
	v_exp_f32_e32 v74, v74
	v_exp_f32_e32 v75, v75
	v_cvt_pk_f16_f32 v172, v72, v73
	v_add_f32_e32 v72, v72, v73
	v_add_f32_e32 v231, v231, v70
	v_mfma_f32_32x32x16_f16 v[32:47], v[200:203], v[164:167], v[32:47]
	ds_read_b128 v[200:203], v226 offset:27744
	buffer_load_dword v222, v250, s[4:7], s25 offen
	v_exp_f32_e32 v76, v76
	v_exp_f32_e32 v77, v77
	v_cvt_pk_f16_f32 v173, v74, v75
	v_add_f32_e32 v74, v74, v75
	v_add_f32_e32 v231, v231, v72
	v_mfma_f32_32x32x16_f16 v[48:63], v[204:207], v[164:167], v[48:63]
	ds_read_b128 v[204:207], v226 offset:32352
	buffer_load_dword v223, v251, s[4:7], s25 offen
	v_exp_f32_e32 v78, v78
	v_exp_f32_e32 v79, v79
	v_cvt_pk_f16_f32 v174, v76, v77
	v_add_f32_e32 v76, v76, v77
	v_add_f32_e32 v231, v231, v74
	v_cvt_pk_f16_f32 v175, v78, v79
	v_add_f32_e32 v78, v78, v79
	v_add_f32_e32 v231, v231, v76
	v_add_f32_e32 v231, v231, v78
	v_cmp_nge_f32_e32 vcc, s34, v231
	s_cbranch_vccnz .Lovf_b1_31

	.amdhsa_kernel _Z8attn_fwdPKfPKiPf
		.amdhsa_group_segment_fixed_size 143360
		.amdhsa_private_segment_fixed_size 0
		.amdhsa_kernarg_size 24
		.amdhsa_user_sgpr_count 2
		.amdhsa_user_sgpr_dispatch_ptr 0
		.amdhsa_user_sgpr_queue_ptr 0
		.amdhsa_user_sgpr_kernarg_segment_ptr 1
		.amdhsa_user_sgpr_dispatch_id 0
		.amdhsa_user_sgpr_kernarg_preload_length 0
		.amdhsa_user_sgpr_kernarg_preload_offset 0
		.amdhsa_user_sgpr_private_segment_size 0
		.amdhsa_uses_dynamic_stack 0
		.amdhsa_enable_private_segment 0
		.amdhsa_system_sgpr_workgroup_id_x 1
		.amdhsa_system_sgpr_workgroup_id_y 0
		.amdhsa_system_sgpr_workgroup_id_z 0
		.amdhsa_system_sgpr_workgroup_info 0
		.amdhsa_system_vgpr_workitem_id 0
		.amdhsa_next_free_vgpr 256
		.amdhsa_next_free_sgpr 56
		.amdhsa_accum_offset 256
		.amdhsa_reserve_vcc 1
		.amdhsa_float_round_mode_32 0
		.amdhsa_float_round_mode_16_64 0
		.amdhsa_float_denorm_mode_32 3
		.amdhsa_float_denorm_mode_16_64 3
		.amdhsa_dx10_clamp 1
		.amdhsa_ieee_mode 1
		.amdhsa_fp16_overflow 0
		.amdhsa_tg_split 0
		.amdhsa_exception_fp_ieee_invalid_op 0
		.amdhsa_exception_fp_denorm_src 0
		.amdhsa_exception_fp_ieee_div_zero 0
		.amdhsa_exception_fp_ieee_overflow 0
		.amdhsa_exception_fp_ieee_underflow 0
		.amdhsa_exception_fp_ieee_inexact 0
		.amdhsa_exception_int_div_zero 0
	.end_amdhsa_kernel

.Lfunc_end0:
	.size	_Z8attn_fwdPKfPKiPf, .Lfunc_end0-_Z8attn_fwdPKfPKiPf
	.set _Z8attn_fwdPKfPKiPf.num_vgpr, 256
	.set _Z8attn_fwdPKfPKiPf.num_agpr, 0
	.set _Z8attn_fwdPKfPKiPf.numbered_sgpr, 56
	.set _Z8attn_fwdPKfPKiPf.num_named_barrier, 0
	.set _Z8attn_fwdPKfPKiPf.private_seg_size, 0
	.set _Z8attn_fwdPKfPKiPf.uses_vcc, 1
	.set _Z8attn_fwdPKfPKiPf.uses_flat_scratch, 0
	.set _Z8attn_fwdPKfPKiPf.has_dyn_sized_stack, 0
	.set _Z8attn_fwdPKfPKiPf.has_recursion, 0
	.set _Z8attn_fwdPKfPKiPf.has_indirect_call, 0

amdhsa.kernels:
  - .agpr_count:     0
    .args:
      - .actual_access:  read_only
        .address_space:  global
        .offset:         0
        .size:           8
        .value_kind:     global_buffer
      - .actual_access:  read_only
        .address_space:  global
        .offset:         8
        .size:           8
        .value_kind:     global_buffer
      - .actual_access:  write_only
        .address_space:  global
        .offset:         16
        .size:           8
        .value_kind:     global_buffer
    .group_segment_fixed_size: 143360
    .kernarg_segment_align: 8
    .kernarg_segment_size: 24
    .language:       OpenCL C
    .language_version:
      - 2
      - 0
    .max_flat_workgroup_size: 512
    .name:           _Z8attn_fwdPKfPKiPf
    .private_segment_fixed_size: 0
    .sgpr_count:     62
    .sgpr_spill_count: 0
    .symbol:         _Z8attn_fwdPKfPKiPf.kd
    .uniform_work_group_size: 1
    .uses_dynamic_stack: false
    .vgpr_count:     256
    .vgpr_spill_count: 0
    .wavefront_size: 64
